# GEMM K-loops: the back-to-back s_setprio 0 / s_setprio 1 pair between the two MFMA groups of a phase removed (priority held through all 16 MFMAs), on top of v34
# baseline (speedup 1.0000x reference)
.LBB0_290:
	s_add_u32 s46, s44, 0xfffc0080
	s_addc_u32 s47, s45, -1
	s_add_i32 s62, 0, 0x10000
	s_cmp_eq_u32 s61, 12
	s_cselect_b32 s49, s1, s47
	s_cselect_b32 s48, s5, s46
	s_cselect_b32 s47, s35, s60
	s_cselect_b32 s46, s37, s59
	s_add_i32 s64, 0, 0x14000
	v_add_u32_e32 v158, s62, v148
	v_add_u32_e32 v174, s64, v148
	ds_read_b128 v[144:147], v158
	ds_read_b128 v[150:153], v158 offset:1024
	ds_read_b128 v[154:157], v158 offset:2048
	ds_read_b128 v[158:161], v158 offset:3072
	ds_read_b128 v[162:165], v174
	ds_read_b128 v[166:169], v174 offset:1024
	ds_read_b128 v[170:173], v174 offset:2048
	ds_read_b128 v[174:177], v174 offset:3072
	v_lshl_add_u64 v[210:211], s[44:45], 0, v[140:141]
	s_add_i32 m0, s50, 0xc000
	ds_read_b128 v[178:181], v149
	ds_read_b128 v[182:185], v149 offset:1024
	ds_read_b128 v[186:189], v149 offset:2048
	ds_read_b128 v[190:193], v149 offset:3072
	ds_read_b128 v[194:197], v149 offset:4096
	ds_read_b128 v[198:201], v149 offset:5120
	ds_read_b128 v[202:205], v149 offset:6144
	ds_read_b128 v[206:209], v149 offset:7168
	global_load_lds_dwordx4 v[210:211], off
	v_lshl_add_u64 v[210:211], s[44:45], 0, v[142:143]
	s_add_i32 m0, s50, 0xe000
	s_nop 0
	global_load_lds_dwordx4 v[210:211], off
	s_waitcnt vmcnt(8)
	s_waitcnt lgkmcnt(0)
	s_barrier
	s_setprio 1
	s_waitcnt lgkmcnt(0)
	v_mfma_f32_16x16x32_bf16 v[130:133], v[144:147], v[178:181], v[130:133]
	v_mfma_f32_16x16x32_bf16 v[126:129], v[154:157], v[178:181], v[126:129]
	v_mfma_f32_16x16x32_bf16 v[114:117], v[144:147], v[186:189], v[114:117]
	v_mfma_f32_16x16x32_bf16 v[110:113], v[154:157], v[186:189], v[110:113]
	v_mfma_f32_16x16x32_bf16 v[98:101], v[144:147], v[194:197], v[98:101]
	v_mfma_f32_16x16x32_bf16 v[94:97], v[154:157], v[194:197], v[94:97]
	v_mfma_f32_16x16x32_bf16 v[82:85], v[144:147], v[202:205], v[82:85]
	v_mfma_f32_16x16x32_bf16 v[78:81], v[154:157], v[202:205], v[78:81]
	v_mfma_f32_16x16x32_bf16 v[130:133], v[150:153], v[182:185], v[130:133]
	v_mfma_f32_16x16x32_bf16 v[126:129], v[158:161], v[182:185], v[126:129]
	v_mfma_f32_16x16x32_bf16 v[114:117], v[150:153], v[190:193], v[114:117]
	v_mfma_f32_16x16x32_bf16 v[110:113], v[158:161], v[190:193], v[110:113]
	v_mfma_f32_16x16x32_bf16 v[98:101], v[150:153], v[198:201], v[98:101]
	v_mfma_f32_16x16x32_bf16 v[94:97], v[158:161], v[198:201], v[94:97]
	v_mfma_f32_16x16x32_bf16 v[82:85], v[150:153], v[206:209], v[82:85]
	v_mfma_f32_16x16x32_bf16 v[78:81], v[158:161], v[206:209], v[78:81]
	v_mfma_f32_16x16x32_bf16 v[122:125], v[162:165], v[178:181], v[122:125]
	v_mfma_f32_16x16x32_bf16 v[118:121], v[170:173], v[178:181], v[118:121]
	v_mfma_f32_16x16x32_bf16 v[106:109], v[162:165], v[186:189], v[106:109]
	v_mfma_f32_16x16x32_bf16 v[102:105], v[170:173], v[186:189], v[102:105]
	v_mfma_f32_16x16x32_bf16 v[90:93], v[162:165], v[194:197], v[90:93]
	v_mfma_f32_16x16x32_bf16 v[86:89], v[170:173], v[194:197], v[86:89]
	v_mfma_f32_16x16x32_bf16 v[74:77], v[162:165], v[202:205], v[74:77]
	v_mfma_f32_16x16x32_bf16 v[70:73], v[170:173], v[202:205], v[70:73]
	v_mfma_f32_16x16x32_bf16 v[122:125], v[166:169], v[182:185], v[122:125]
	v_mfma_f32_16x16x32_bf16 v[118:121], v[174:177], v[182:185], v[118:121]
	v_mfma_f32_16x16x32_bf16 v[106:109], v[166:169], v[190:193], v[106:109]
	v_mfma_f32_16x16x32_bf16 v[102:105], v[174:177], v[190:193], v[102:105]
	v_mfma_f32_16x16x32_bf16 v[90:93], v[166:169], v[198:201], v[90:93]
	v_mfma_f32_16x16x32_bf16 v[86:89], v[174:177], v[198:201], v[86:89]
	v_mfma_f32_16x16x32_bf16 v[74:77], v[166:169], v[206:209], v[74:77]
	v_mfma_f32_16x16x32_bf16 v[70:73], v[174:177], v[206:209], v[70:73]
	s_setprio 0
	s_barrier
	s_add_i32 s62, s62, s27
	v_lshl_add_u64 v[210:211], s[46:47], 0, v[0:1]
	s_mov_b32 m0, s62
	ds_read_b128 v[178:181], v149 offset:16384
	ds_read_b128 v[182:185], v149 offset:17408
	ds_read_b128 v[186:189], v149 offset:18432
	ds_read_b128 v[190:193], v149 offset:19456
	ds_read_b128 v[194:197], v149 offset:20480
	ds_read_b128 v[198:201], v149 offset:21504
	ds_read_b128 v[202:205], v149 offset:22528
	ds_read_b128 v[206:209], v149 offset:23552
	global_load_lds_dwordx4 v[210:211], off
	s_add_i32 m0, s62, 0x2000
	s_add_u32 s62, s46, 0x40000
	v_lshl_add_u64 v[212:213], s[46:47], 0, v[138:139]
	s_addc_u32 s63, s47, 0
	s_add_i32 s64, s64, s27
	global_load_lds_dwordx4 v[212:213], off
	v_lshl_add_u64 v[216:217], s[62:63], 0, v[0:1]
	s_mov_b32 m0, s64
	v_lshl_add_u64 v[218:219], s[48:49], 0, v[136:137]
	global_load_lds_dwordx4 v[216:217], off
	v_lshl_add_u64 v[216:217], s[62:63], 0, v[138:139]
	s_add_i32 m0, s64, 0x2000
	s_nop 0
	global_load_lds_dwordx4 v[216:217], off
	v_lshl_add_u64 v[216:217], s[48:49], 0, v[134:135]
	s_mov_b32 m0, s50
	s_nop 0
	global_load_lds_dwordx4 v[216:217], off
	s_mov_b32 m0, s51
	s_nop 0
	global_load_lds_dwordx4 v[218:219], off
	s_waitcnt vmcnt(8)
	s_waitcnt lgkmcnt(0)
	s_barrier
	s_setprio 1
	s_waitcnt lgkmcnt(0)
	v_mfma_f32_16x16x32_bf16 v[66:69], v[144:147], v[178:181], v[66:69]
	v_mfma_f32_16x16x32_bf16 v[62:65], v[154:157], v[178:181], v[62:65]
	v_mfma_f32_16x16x32_bf16 v[50:53], v[144:147], v[186:189], v[50:53]
	v_mfma_f32_16x16x32_bf16 v[46:49], v[154:157], v[186:189], v[46:49]
	v_mfma_f32_16x16x32_bf16 v[34:37], v[144:147], v[194:197], v[34:37]
	v_mfma_f32_16x16x32_bf16 v[30:33], v[154:157], v[194:197], v[30:33]
	v_mfma_f32_16x16x32_bf16 v[18:21], v[144:147], v[202:205], v[18:21]
	v_mfma_f32_16x16x32_bf16 v[14:17], v[154:157], v[202:205], v[14:17]
	v_mfma_f32_16x16x32_bf16 v[66:69], v[150:153], v[182:185], v[66:69]
	v_mfma_f32_16x16x32_bf16 v[62:65], v[158:161], v[182:185], v[62:65]
	v_mfma_f32_16x16x32_bf16 v[50:53], v[150:153], v[190:193], v[50:53]
	v_mfma_f32_16x16x32_bf16 v[46:49], v[158:161], v[190:193], v[46:49]
	v_mfma_f32_16x16x32_bf16 v[34:37], v[150:153], v[198:201], v[34:37]
	v_mfma_f32_16x16x32_bf16 v[30:33], v[158:161], v[198:201], v[30:33]
	v_mfma_f32_16x16x32_bf16 v[18:21], v[150:153], v[206:209], v[18:21]
	v_mfma_f32_16x16x32_bf16 v[14:17], v[158:161], v[206:209], v[14:17]
	v_mfma_f32_16x16x32_bf16 v[58:61], v[162:165], v[178:181], v[58:61]
	v_mfma_f32_16x16x32_bf16 v[54:57], v[170:173], v[178:181], v[54:57]
	v_mfma_f32_16x16x32_bf16 v[42:45], v[162:165], v[186:189], v[42:45]
	v_mfma_f32_16x16x32_bf16 v[38:41], v[170:173], v[186:189], v[38:41]
	v_mfma_f32_16x16x32_bf16 v[26:29], v[162:165], v[194:197], v[26:29]
	v_mfma_f32_16x16x32_bf16 v[22:25], v[170:173], v[194:197], v[22:25]
	v_mfma_f32_16x16x32_bf16 v[10:13], v[162:165], v[202:205], v[10:13]
	v_mfma_f32_16x16x32_bf16 v[6:9], v[170:173], v[202:205], v[6:9]
	v_mfma_f32_16x16x32_bf16 v[58:61], v[166:169], v[182:185], v[58:61]
	v_mfma_f32_16x16x32_bf16 v[54:57], v[174:177], v[182:185], v[54:57]
	v_mfma_f32_16x16x32_bf16 v[42:45], v[166:169], v[190:193], v[42:45]
	v_mfma_f32_16x16x32_bf16 v[38:41], v[174:177], v[190:193], v[38:41]
	v_mfma_f32_16x16x32_bf16 v[26:29], v[166:169], v[198:201], v[26:29]
	v_mfma_f32_16x16x32_bf16 v[22:25], v[174:177], v[198:201], v[22:25]
	v_mfma_f32_16x16x32_bf16 v[10:13], v[166:169], v[206:209], v[10:13]
	v_mfma_f32_16x16x32_bf16 v[6:9], v[174:177], v[206:209], v[6:9]
	s_setprio 0
	s_barrier
	s_add_i32 s62, 0, 0x18000
	s_add_i32 s63, 0, 0x1c000
	v_add_u32_e32 v158, s62, v148
	v_add_u32_e32 v174, s63, v148
	ds_read_b128 v[144:147], v158
	ds_read_b128 v[150:153], v158 offset:1024
	ds_read_b128 v[154:157], v158 offset:2048
	ds_read_b128 v[158:161], v158 offset:3072
	ds_read_b128 v[162:165], v174
	ds_read_b128 v[166:169], v174 offset:1024
	ds_read_b128 v[170:173], v174 offset:2048
	ds_read_b128 v[174:177], v174 offset:3072
	s_add_u32 s48, s48, 0x40000
	s_addc_u32 s49, s49, 0
	s_mov_b32 m0, s52
	v_lshl_add_u64 v[220:221], s[48:49], 0, v[134:135]
	ds_read_b128 v[178:181], v149 offset:32768
	ds_read_b128 v[182:185], v149 offset:33792
	ds_read_b128 v[186:189], v149 offset:34816
	ds_read_b128 v[190:193], v149 offset:35840
	ds_read_b128 v[194:197], v149 offset:36864
	ds_read_b128 v[198:201], v149 offset:37888
	ds_read_b128 v[202:205], v149 offset:38912
	ds_read_b128 v[206:209], v149 offset:39936
	global_load_lds_dwordx4 v[220:221], off
	v_lshl_add_u64 v[220:221], s[48:49], 0, v[136:137]
	s_mov_b32 m0, s53
	s_nop 0
	global_load_lds_dwordx4 v[220:221], off
	s_waitcnt vmcnt(8)
	s_waitcnt lgkmcnt(0)
	s_barrier
	s_setprio 1
	s_waitcnt lgkmcnt(0)
	v_mfma_f32_16x16x32_bf16 v[130:133], v[144:147], v[178:181], v[130:133]
	v_mfma_f32_16x16x32_bf16 v[126:129], v[154:157], v[178:181], v[126:129]
	v_mfma_f32_16x16x32_bf16 v[114:117], v[144:147], v[186:189], v[114:117]
	v_mfma_f32_16x16x32_bf16 v[110:113], v[154:157], v[186:189], v[110:113]
	v_mfma_f32_16x16x32_bf16 v[98:101], v[144:147], v[194:197], v[98:101]
	v_mfma_f32_16x16x32_bf16 v[94:97], v[154:157], v[194:197], v[94:97]
	v_mfma_f32_16x16x32_bf16 v[82:85], v[144:147], v[202:205], v[82:85]
	v_mfma_f32_16x16x32_bf16 v[78:81], v[154:157], v[202:205], v[78:81]
	v_mfma_f32_16x16x32_bf16 v[130:133], v[150:153], v[182:185], v[130:133]
	v_mfma_f32_16x16x32_bf16 v[126:129], v[158:161], v[182:185], v[126:129]
	v_mfma_f32_16x16x32_bf16 v[114:117], v[150:153], v[190:193], v[114:117]
	v_mfma_f32_16x16x32_bf16 v[110:113], v[158:161], v[190:193], v[110:113]
	v_mfma_f32_16x16x32_bf16 v[98:101], v[150:153], v[198:201], v[98:101]
	v_mfma_f32_16x16x32_bf16 v[94:97], v[158:161], v[198:201], v[94:97]
	v_mfma_f32_16x16x32_bf16 v[82:85], v[150:153], v[206:209], v[82:85]
	v_mfma_f32_16x16x32_bf16 v[78:81], v[158:161], v[206:209], v[78:81]
	v_mfma_f32_16x16x32_bf16 v[122:125], v[162:165], v[178:181], v[122:125]
	v_mfma_f32_16x16x32_bf16 v[118:121], v[170:173], v[178:181], v[118:121]
	v_mfma_f32_16x16x32_bf16 v[106:109], v[162:165], v[186:189], v[106:109]
	v_mfma_f32_16x16x32_bf16 v[102:105], v[170:173], v[186:189], v[102:105]
	v_mfma_f32_16x16x32_bf16 v[90:93], v[162:165], v[194:197], v[90:93]
	v_mfma_f32_16x16x32_bf16 v[86:89], v[170:173], v[194:197], v[86:89]
	v_mfma_f32_16x16x32_bf16 v[74:77], v[162:165], v[202:205], v[74:77]
	v_mfma_f32_16x16x32_bf16 v[70:73], v[170:173], v[202:205], v[70:73]
	v_mfma_f32_16x16x32_bf16 v[122:125], v[166:169], v[182:185], v[122:125]
	v_mfma_f32_16x16x32_bf16 v[118:121], v[174:177], v[182:185], v[118:121]
	v_mfma_f32_16x16x32_bf16 v[106:109], v[166:169], v[190:193], v[106:109]
	v_mfma_f32_16x16x32_bf16 v[102:105], v[174:177], v[190:193], v[102:105]
	v_mfma_f32_16x16x32_bf16 v[90:93], v[166:169], v[198:201], v[90:93]
	v_mfma_f32_16x16x32_bf16 v[86:89], v[174:177], v[198:201], v[86:89]
	v_mfma_f32_16x16x32_bf16 v[74:77], v[166:169], v[206:209], v[74:77]
	v_mfma_f32_16x16x32_bf16 v[70:73], v[174:177], v[206:209], v[70:73]
	s_setprio 0
	s_barrier
	s_add_i32 s48, s62, s27
	v_lshl_add_u64 v[210:211], v[210:211], 0, s[66:67]
	s_mov_b32 m0, s48
	ds_read_b128 v[178:181], v149 offset:49152
	ds_read_b128 v[182:185], v149 offset:50176
	ds_read_b128 v[186:189], v149 offset:51200
	ds_read_b128 v[190:193], v149 offset:52224
	ds_read_b128 v[194:197], v149 offset:53248
	ds_read_b128 v[198:201], v149 offset:54272
	ds_read_b128 v[202:205], v149 offset:55296
	ds_read_b128 v[206:209], v149 offset:56320
	global_load_lds_dwordx4 v[210:211], off
	s_add_i32 m0, s48, 0x2000
	s_add_u32 s46, s46, 0x40080
	v_lshl_add_u64 v[210:211], v[212:213], 0, s[66:67]
	s_addc_u32 s47, s47, 0
	s_add_i32 s48, s63, s27
	global_load_lds_dwordx4 v[210:211], off
	v_lshl_add_u64 v[210:211], s[46:47], 0, v[0:1]
	s_mov_b32 m0, s48
	s_nop 0
	global_load_lds_dwordx4 v[210:211], off
	v_lshl_add_u64 v[210:211], s[46:47], 0, v[138:139]
	s_add_i32 m0, s48, 0x2000
	s_nop 0
	global_load_lds_dwordx4 v[210:211], off
	v_lshl_add_u64 v[210:211], v[216:217], 0, s[66:67]
	s_mov_b32 m0, s56
	s_nop 0
	global_load_lds_dwordx4 v[210:211], off
	v_lshl_add_u64 v[210:211], v[218:219], 0, s[66:67]
	s_mov_b32 m0, s57
	s_nop 0
	global_load_lds_dwordx4 v[210:211], off
	s_waitcnt vmcnt(8)
	s_waitcnt lgkmcnt(0)
	s_barrier
	s_setprio 1
	s_waitcnt lgkmcnt(0)
	v_mfma_f32_16x16x32_bf16 v[66:69], v[144:147], v[178:181], v[66:69]
	v_mfma_f32_16x16x32_bf16 v[62:65], v[154:157], v[178:181], v[62:65]
	v_mfma_f32_16x16x32_bf16 v[50:53], v[144:147], v[186:189], v[50:53]
	v_mfma_f32_16x16x32_bf16 v[46:49], v[154:157], v[186:189], v[46:49]
	v_mfma_f32_16x16x32_bf16 v[34:37], v[144:147], v[194:197], v[34:37]
	v_mfma_f32_16x16x32_bf16 v[30:33], v[154:157], v[194:197], v[30:33]
	v_mfma_f32_16x16x32_bf16 v[18:21], v[144:147], v[202:205], v[18:21]
	v_mfma_f32_16x16x32_bf16 v[14:17], v[154:157], v[202:205], v[14:17]
	v_mfma_f32_16x16x32_bf16 v[66:69], v[150:153], v[182:185], v[66:69]
	v_mfma_f32_16x16x32_bf16 v[62:65], v[158:161], v[182:185], v[62:65]
	v_mfma_f32_16x16x32_bf16 v[50:53], v[150:153], v[190:193], v[50:53]
	v_mfma_f32_16x16x32_bf16 v[46:49], v[158:161], v[190:193], v[46:49]
	v_mfma_f32_16x16x32_bf16 v[34:37], v[150:153], v[198:201], v[34:37]
	v_mfma_f32_16x16x32_bf16 v[30:33], v[158:161], v[198:201], v[30:33]
	v_mfma_f32_16x16x32_bf16 v[18:21], v[150:153], v[206:209], v[18:21]
	v_mfma_f32_16x16x32_bf16 v[14:17], v[158:161], v[206:209], v[14:17]
	v_mfma_f32_16x16x32_bf16 v[58:61], v[162:165], v[178:181], v[58:61]
	v_mfma_f32_16x16x32_bf16 v[54:57], v[170:173], v[178:181], v[54:57]
	v_mfma_f32_16x16x32_bf16 v[42:45], v[162:165], v[186:189], v[42:45]
	v_mfma_f32_16x16x32_bf16 v[38:41], v[170:173], v[186:189], v[38:41]
	v_mfma_f32_16x16x32_bf16 v[26:29], v[162:165], v[194:197], v[26:29]
	v_mfma_f32_16x16x32_bf16 v[22:25], v[170:173], v[194:197], v[22:25]
	v_mfma_f32_16x16x32_bf16 v[10:13], v[162:165], v[202:205], v[10:13]
	v_mfma_f32_16x16x32_bf16 v[6:9], v[170:173], v[202:205], v[6:9]
	v_mfma_f32_16x16x32_bf16 v[58:61], v[166:169], v[182:185], v[58:61]
	v_mfma_f32_16x16x32_bf16 v[54:57], v[174:177], v[182:185], v[54:57]
	v_mfma_f32_16x16x32_bf16 v[42:45], v[166:169], v[190:193], v[42:45]
	v_mfma_f32_16x16x32_bf16 v[38:41], v[174:177], v[190:193], v[38:41]
	v_mfma_f32_16x16x32_bf16 v[26:29], v[166:169], v[198:201], v[26:29]
	v_mfma_f32_16x16x32_bf16 v[22:25], v[174:177], v[198:201], v[22:25]
	v_mfma_f32_16x16x32_bf16 v[10:13], v[166:169], v[206:209], v[10:13]
	v_mfma_f32_16x16x32_bf16 v[6:9], v[174:177], v[206:209], v[6:9]
	s_setprio 0
	s_barrier
	s_add_i32 s61, s61, 2
	s_add_u32 s44, s44, 0x100
	s_addc_u32 s45, s45, 0
	s_add_u32 s59, s59, 0x100
	s_addc_u32 s60, s60, 0
	s_cmp_gt_u32 s61, 13
	s_cbranch_scc0 .LBB0_290
	s_and_b64 vcc, exec, s[30:31]
	s_cbranch_vccz .LBB0_293
	s_barrier

.Lrw_done_ip8_0:
	s_waitcnt lgkmcnt(0)
	s_barrier
	s_setprio 1
	s_waitcnt lgkmcnt(0)
	v_mfma_scale_f32_16x16x128_f8f6f4 v[158:161], v[18:25], v[172:179], 0, v234, v235 op_sel_hi:[0,0,0]
	v_mfma_scale_f32_16x16x128_f8f6f4 v[154:157], v[26:33], v[172:179], 0, v234, v235 op_sel_hi:[0,0,0]
	v_mfma_scale_f32_16x16x128_f8f6f4 v[150:153], v[18:25], v[198:205], 0, v234, v235 op_sel_hi:[0,0,0]
	v_mfma_scale_f32_16x16x128_f8f6f4 v[146:149], v[26:33], v[198:205], 0, v234, v235 op_sel_hi:[0,0,0]
	v_mfma_scale_f32_16x16x128_f8f6f4 v[142:145], v[18:25], v[206:213], 0, v234, v235 op_sel_hi:[0,0,0]
	v_mfma_scale_f32_16x16x128_f8f6f4 v[138:141], v[26:33], v[206:213], 0, v234, v235 op_sel_hi:[0,0,0]
	v_mfma_scale_f32_16x16x128_f8f6f4 v[134:137], v[18:25], v[216:223], 0, v234, v235 op_sel_hi:[0,0,0]
	v_mfma_scale_f32_16x16x128_f8f6f4 v[130:133], v[26:33], v[216:223], 0, v234, v235 op_sel_hi:[0,0,0]
	v_mfma_scale_f32_16x16x128_f8f6f4 v[126:129], v[2:9], v[172:179], 0, v234, v235 op_sel_hi:[0,0,0]
	v_mfma_scale_f32_16x16x128_f8f6f4 v[122:125], v[10:17], v[172:179], 0, v234, v235 op_sel_hi:[0,0,0]
	v_mfma_scale_f32_16x16x128_f8f6f4 v[118:121], v[2:9], v[198:205], 0, v234, v235 op_sel_hi:[0,0,0]
	v_mfma_scale_f32_16x16x128_f8f6f4 v[114:117], v[10:17], v[198:205], 0, v234, v235 op_sel_hi:[0,0,0]
	v_mfma_scale_f32_16x16x128_f8f6f4 v[110:113], v[2:9], v[206:213], 0, v234, v235 op_sel_hi:[0,0,0]
	v_mfma_scale_f32_16x16x128_f8f6f4 v[106:109], v[10:17], v[206:213], 0, v234, v235 op_sel_hi:[0,0,0]
	v_mfma_scale_f32_16x16x128_f8f6f4 v[102:105], v[2:9], v[216:223], 0, v234, v235 op_sel_hi:[0,0,0]
	v_mfma_scale_f32_16x16x128_f8f6f4 v[98:101], v[10:17], v[216:223], 0, v234, v235 op_sel_hi:[0,0,0]
	s_setprio 0
	s_barrier
	v_lshl_add_u64 v[172:173], s[44:45], 0, v[0:1]
	s_mov_b64 s[74:75], 0x100
	s_mov_b32 m0, s58
	v_lshl_add_u64 v[174:175], v[172:173], 0, s[74:75]
	ds_read_b128 v[198:201], v196 offset:16384
	ds_read_b128 v[202:205], v196 offset:17408
	ds_read_b128 v[206:209], v196 offset:18432
	ds_read_b128 v[210:213], v196 offset:19456
	ds_read_b128 v[216:219], v196 offset:20480
	ds_read_b128 v[220:223], v196 offset:21504
	ds_read_b128 v[224:227], v196 offset:22528
	ds_read_b128 v[228:231], v196 offset:23552
	global_load_lds_dwordx4 v[174:175], off
	v_lshl_add_u64 v[174:175], s[44:45], 0, v[166:167]
	s_add_u32 s48, s44, 0x20100
	v_lshl_add_u64 v[176:177], v[174:175], 0, s[74:75]
	s_mov_b32 m0, s59
	s_addc_u32 s49, s45, 0
	global_load_lds_dwordx4 v[176:177], off
	v_lshl_add_u64 v[176:177], s[48:49], 0, v[0:1]
	s_mov_b32 m0, s60
	s_nop 0
	global_load_lds_dwordx4 v[176:177], off
	v_lshl_add_u64 v[176:177], s[48:49], 0, v[166:167]
	s_mov_b32 m0, s61
	s_nop 0
	global_load_lds_dwordx4 v[176:177], off
	v_lshl_add_u64 v[176:177], s[46:47], 0, v[162:163]
	v_lshl_add_u64 v[178:179], v[176:177], 0, s[74:75]
	s_mov_b32 m0, s57
	s_nop 0
	global_load_lds_dwordx4 v[178:179], off
	v_lshl_add_u64 v[178:179], s[46:47], 0, v[164:165]
	v_lshl_add_u64 v[232:233], v[178:179], 0, s[74:75]
	s_mov_b32 m0, s62
	s_nop 0
	global_load_lds_dwordx4 v[232:233], off
	s_cmp_eq_u32 s50, 1
	s_cbranch_scc1 .Lrw_first_ip8_1
	s_waitcnt vmcnt(24)
	s_branch .Lrw_done_ip8_1

.Lrw_done_ip8_1:
	s_waitcnt lgkmcnt(0)
	s_barrier
	s_setprio 1
	s_waitcnt lgkmcnt(0)
	v_mfma_scale_f32_16x16x128_f8f6f4 v[94:97], v[18:25], v[198:205], 0, v234, v235 op_sel_hi:[0,0,0]
	v_mfma_scale_f32_16x16x128_f8f6f4 v[90:93], v[26:33], v[198:205], 0, v234, v235 op_sel_hi:[0,0,0]
	v_mfma_scale_f32_16x16x128_f8f6f4 v[86:89], v[18:25], v[206:213], 0, v234, v235 op_sel_hi:[0,0,0]
	v_mfma_scale_f32_16x16x128_f8f6f4 v[82:85], v[26:33], v[206:213], 0, v234, v235 op_sel_hi:[0,0,0]
	v_mfma_scale_f32_16x16x128_f8f6f4 v[78:81], v[18:25], v[216:223], 0, v234, v235 op_sel_hi:[0,0,0]
	v_mfma_scale_f32_16x16x128_f8f6f4 v[74:77], v[26:33], v[216:223], 0, v234, v235 op_sel_hi:[0,0,0]
	v_mfma_scale_f32_16x16x128_f8f6f4 v[70:73], v[18:25], v[224:231], 0, v234, v235 op_sel_hi:[0,0,0]
	v_mfma_scale_f32_16x16x128_f8f6f4 v[66:69], v[26:33], v[224:231], 0, v234, v235 op_sel_hi:[0,0,0]
	v_mfma_scale_f32_16x16x128_f8f6f4 v[62:65], v[2:9], v[198:205], 0, v234, v235 op_sel_hi:[0,0,0]
	v_mfma_scale_f32_16x16x128_f8f6f4 v[58:61], v[10:17], v[198:205], 0, v234, v235 op_sel_hi:[0,0,0]
	v_mfma_scale_f32_16x16x128_f8f6f4 v[54:57], v[2:9], v[206:213], 0, v234, v235 op_sel_hi:[0,0,0]
	v_mfma_scale_f32_16x16x128_f8f6f4 v[50:53], v[10:17], v[206:213], 0, v234, v235 op_sel_hi:[0,0,0]
	v_mfma_scale_f32_16x16x128_f8f6f4 v[46:49], v[2:9], v[216:223], 0, v234, v235 op_sel_hi:[0,0,0]
	v_mfma_scale_f32_16x16x128_f8f6f4 v[42:45], v[10:17], v[216:223], 0, v234, v235 op_sel_hi:[0,0,0]
	v_mfma_scale_f32_16x16x128_f8f6f4 v[38:41], v[2:9], v[224:231], 0, v234, v235 op_sel_hi:[0,0,0]
	v_mfma_scale_f32_16x16x128_f8f6f4 v[34:37], v[10:17], v[224:231], 0, v234, v235 op_sel_hi:[0,0,0]
	s_setprio 0
	s_barrier
	ds_read_b128 v[18:21], v188
	ds_read_b128 v[22:25], v189
	ds_read_b128 v[26:29], v190
	ds_read_b128 v[30:33], v191
	ds_read_b128 v[2:5], v192
	ds_read_b128 v[6:9], v193
	ds_read_b128 v[10:13], v194
	ds_read_b128 v[14:17], v195
	s_add_u32 s48, s46, 0x20100
	s_addc_u32 s49, s47, 0
	s_mov_b32 m0, s63
	v_lshl_add_u64 v[232:233], s[48:49], 0, v[162:163]
	ds_read_b128 v[198:201], v196 offset:32768
	ds_read_b128 v[202:205], v196 offset:33792
	ds_read_b128 v[206:209], v196 offset:34816
	ds_read_b128 v[210:213], v196 offset:35840
	ds_read_b128 v[216:219], v196 offset:36864
	ds_read_b128 v[220:223], v196 offset:37888
	ds_read_b128 v[224:227], v196 offset:38912
	ds_read_b128 v[228:231], v196 offset:39936
	global_load_lds_dwordx4 v[232:233], off
	v_lshl_add_u64 v[232:233], s[48:49], 0, v[164:165]
	s_mov_b32 m0, s64
	s_nop 0
	global_load_lds_dwordx4 v[232:233], off
	s_waitcnt vmcnt(8)
	s_waitcnt lgkmcnt(0)
	s_barrier
	s_setprio 1
	s_waitcnt lgkmcnt(0)
	v_mfma_scale_f32_16x16x128_f8f6f4 v[158:161], v[18:25], v[198:205], v[158:161], v234, v235 op_sel_hi:[0,0,0]
	v_mfma_scale_f32_16x16x128_f8f6f4 v[154:157], v[26:33], v[198:205], v[154:157], v234, v235 op_sel_hi:[0,0,0]
	v_mfma_scale_f32_16x16x128_f8f6f4 v[150:153], v[18:25], v[206:213], v[150:153], v234, v235 op_sel_hi:[0,0,0]
	v_mfma_scale_f32_16x16x128_f8f6f4 v[146:149], v[26:33], v[206:213], v[146:149], v234, v235 op_sel_hi:[0,0,0]
	v_mfma_scale_f32_16x16x128_f8f6f4 v[142:145], v[18:25], v[216:223], v[142:145], v234, v235 op_sel_hi:[0,0,0]
	v_mfma_scale_f32_16x16x128_f8f6f4 v[138:141], v[26:33], v[216:223], v[138:141], v234, v235 op_sel_hi:[0,0,0]
	v_mfma_scale_f32_16x16x128_f8f6f4 v[134:137], v[18:25], v[224:231], v[134:137], v234, v235 op_sel_hi:[0,0,0]
	v_mfma_scale_f32_16x16x128_f8f6f4 v[130:133], v[26:33], v[224:231], v[130:133], v234, v235 op_sel_hi:[0,0,0]
	v_mfma_scale_f32_16x16x128_f8f6f4 v[126:129], v[2:9], v[198:205], v[126:129], v234, v235 op_sel_hi:[0,0,0]
	v_mfma_scale_f32_16x16x128_f8f6f4 v[122:125], v[10:17], v[198:205], v[122:125], v234, v235 op_sel_hi:[0,0,0]
	v_mfma_scale_f32_16x16x128_f8f6f4 v[118:121], v[2:9], v[206:213], v[118:121], v234, v235 op_sel_hi:[0,0,0]
	v_mfma_scale_f32_16x16x128_f8f6f4 v[114:117], v[10:17], v[206:213], v[114:117], v234, v235 op_sel_hi:[0,0,0]
	v_mfma_scale_f32_16x16x128_f8f6f4 v[110:113], v[2:9], v[216:223], v[110:113], v234, v235 op_sel_hi:[0,0,0]
	v_mfma_scale_f32_16x16x128_f8f6f4 v[106:109], v[10:17], v[216:223], v[106:109], v234, v235 op_sel_hi:[0,0,0]
	v_mfma_scale_f32_16x16x128_f8f6f4 v[102:105], v[2:9], v[224:231], v[102:105], v234, v235 op_sel_hi:[0,0,0]
	v_mfma_scale_f32_16x16x128_f8f6f4 v[98:101], v[10:17], v[224:231], v[98:101], v234, v235 op_sel_hi:[0,0,0]
	s_setprio 0
	s_barrier
	s_mov_b64 s[74:75], 0x180
	s_mov_b32 m0, s7
	v_lshl_add_u64 v[172:173], v[172:173], 0, s[74:75]
	s_add_u32 s48, s44, 0x20180
	ds_read_b128 v[198:201], v196 offset:49152
	ds_read_b128 v[202:205], v196 offset:50176
	ds_read_b128 v[206:209], v196 offset:51200
	ds_read_b128 v[210:213], v196 offset:52224
	ds_read_b128 v[216:219], v196 offset:53248
	ds_read_b128 v[220:223], v196 offset:54272
	ds_read_b128 v[224:227], v196 offset:55296
	ds_read_b128 v[228:231], v196 offset:56320
	global_load_lds_dwordx4 v[172:173], off
	v_lshl_add_u64 v[172:173], v[174:175], 0, s[74:75]
	s_mov_b32 m0, s65
	s_addc_u32 s49, s45, 0
	global_load_lds_dwordx4 v[172:173], off
	v_lshl_add_u64 v[172:173], s[48:49], 0, v[0:1]
	s_mov_b32 m0, s13
	s_nop 0
	global_load_lds_dwordx4 v[172:173], off
	v_lshl_add_u64 v[172:173], s[48:49], 0, v[166:167]
	s_mov_b32 m0, s51
	s_nop 0
	global_load_lds_dwordx4 v[172:173], off
	v_lshl_add_u64 v[172:173], v[176:177], 0, s[74:75]
	s_mov_b32 m0, s68
	s_nop 0
	global_load_lds_dwordx4 v[172:173], off
	v_lshl_add_u64 v[172:173], v[178:179], 0, s[74:75]
	s_mov_b32 m0, s52
	s_nop 0
	global_load_lds_dwordx4 v[172:173], off
	s_waitcnt vmcnt(8)
	s_waitcnt lgkmcnt(0)
	s_barrier
	s_setprio 1
	s_waitcnt lgkmcnt(0)
	v_mfma_scale_f32_16x16x128_f8f6f4 v[94:97], v[18:25], v[198:205], v[94:97], v234, v235 op_sel_hi:[0,0,0]
	v_mfma_scale_f32_16x16x128_f8f6f4 v[90:93], v[26:33], v[198:205], v[90:93], v234, v235 op_sel_hi:[0,0,0]
	v_mfma_scale_f32_16x16x128_f8f6f4 v[86:89], v[18:25], v[206:213], v[86:89], v234, v235 op_sel_hi:[0,0,0]
	v_mfma_scale_f32_16x16x128_f8f6f4 v[82:85], v[26:33], v[206:213], v[82:85], v234, v235 op_sel_hi:[0,0,0]
	v_mfma_scale_f32_16x16x128_f8f6f4 v[78:81], v[18:25], v[216:223], v[78:81], v234, v235 op_sel_hi:[0,0,0]
	v_mfma_scale_f32_16x16x128_f8f6f4 v[74:77], v[26:33], v[216:223], v[74:77], v234, v235 op_sel_hi:[0,0,0]
	v_mfma_scale_f32_16x16x128_f8f6f4 v[70:73], v[18:25], v[224:231], v[70:73], v234, v235 op_sel_hi:[0,0,0]
	v_mfma_scale_f32_16x16x128_f8f6f4 v[66:69], v[26:33], v[224:231], v[66:69], v234, v235 op_sel_hi:[0,0,0]
	v_mfma_scale_f32_16x16x128_f8f6f4 v[62:65], v[2:9], v[198:205], v[62:65], v234, v235 op_sel_hi:[0,0,0]
	v_mfma_scale_f32_16x16x128_f8f6f4 v[58:61], v[10:17], v[198:205], v[58:61], v234, v235 op_sel_hi:[0,0,0]
	v_mfma_scale_f32_16x16x128_f8f6f4 v[54:57], v[2:9], v[206:213], v[54:57], v234, v235 op_sel_hi:[0,0,0]
	v_mfma_scale_f32_16x16x128_f8f6f4 v[50:53], v[10:17], v[206:213], v[50:53], v234, v235 op_sel_hi:[0,0,0]
	v_mfma_scale_f32_16x16x128_f8f6f4 v[46:49], v[2:9], v[216:223], v[46:49], v234, v235 op_sel_hi:[0,0,0]
	v_mfma_scale_f32_16x16x128_f8f6f4 v[42:45], v[10:17], v[216:223], v[42:45], v234, v235 op_sel_hi:[0,0,0]
	v_mfma_scale_f32_16x16x128_f8f6f4 v[38:41], v[2:9], v[224:231], v[38:41], v234, v235 op_sel_hi:[0,0,0]
	v_mfma_scale_f32_16x16x128_f8f6f4 v[34:37], v[10:17], v[224:231], v[34:37], v234, v235 op_sel_hi:[0,0,0]
	s_setprio 0
	s_barrier
	s_add_u32 s46, s46, 0x20180
	s_addc_u32 s47, s47, 0
	s_add_u32 s37, s44, 0x200
	s_addc_u32 s74, s45, 0
	s_mov_b32 s75, 0
.LBB0_388:
	ds_read_b128 v[2:5], v180
	ds_read_b128 v[6:9], v181
	ds_read_b128 v[10:13], v182
	ds_read_b128 v[14:17], v183
	ds_read_b128 v[26:29], v184
	ds_read_b128 v[30:33], v185
	ds_read_b128 v[172:175], v186
	ds_read_b128 v[176:179], v187
	s_add_u32 s44, s46, 0xfffe0080
	s_addc_u32 s45, s47, -1
	s_cmp_eq_u32 s75, 4
	s_cselect_b32 s49, s1, s45
	s_cselect_b32 s48, s5, s44
	s_cselect_b32 s45, s23, s74
	s_cselect_b32 s44, s26, s37
	s_mov_b32 m0, s27
	v_lshl_add_u64 v[224:225], s[46:47], 0, v[168:169]
	ds_read_b128 v[18:21], v196
	ds_read_b128 v[22:25], v196 offset:1024
	ds_read_b128 v[198:201], v196 offset:2048
	ds_read_b128 v[202:205], v196 offset:3072
	ds_read_b128 v[206:209], v196 offset:4096
	ds_read_b128 v[210:213], v196 offset:5120
	ds_read_b128 v[216:219], v196 offset:6144
	ds_read_b128 v[220:223], v196 offset:7168
	global_load_lds_dwordx4 v[224:225], off
	v_lshl_add_u64 v[224:225], s[46:47], 0, v[170:171]
	s_mov_b32 m0, s35
	s_nop 0
	global_load_lds_dwordx4 v[224:225], off
	s_waitcnt vmcnt(8)
	s_waitcnt lgkmcnt(0)
	s_barrier
	s_setprio 1
	s_waitcnt lgkmcnt(0)
	v_mfma_scale_f32_16x16x128_f8f6f4 v[158:161], v[2:9], v[18:25], v[158:161], v234, v235 op_sel_hi:[0,0,0]
	v_mfma_scale_f32_16x16x128_f8f6f4 v[154:157], v[10:17], v[18:25], v[154:157], v234, v235 op_sel_hi:[0,0,0]
	v_mfma_scale_f32_16x16x128_f8f6f4 v[150:153], v[2:9], v[198:205], v[150:153], v234, v235 op_sel_hi:[0,0,0]
	v_mfma_scale_f32_16x16x128_f8f6f4 v[146:149], v[10:17], v[198:205], v[146:149], v234, v235 op_sel_hi:[0,0,0]
	v_mfma_scale_f32_16x16x128_f8f6f4 v[142:145], v[2:9], v[206:213], v[142:145], v234, v235 op_sel_hi:[0,0,0]
	v_mfma_scale_f32_16x16x128_f8f6f4 v[138:141], v[10:17], v[206:213], v[138:141], v234, v235 op_sel_hi:[0,0,0]
	v_mfma_scale_f32_16x16x128_f8f6f4 v[134:137], v[2:9], v[216:223], v[134:137], v234, v235 op_sel_hi:[0,0,0]
	v_mfma_scale_f32_16x16x128_f8f6f4 v[130:133], v[10:17], v[216:223], v[130:133], v234, v235 op_sel_hi:[0,0,0]
	v_mfma_scale_f32_16x16x128_f8f6f4 v[126:129], v[26:33], v[18:25], v[126:129], v234, v235 op_sel_hi:[0,0,0]
	v_mfma_scale_f32_16x16x128_f8f6f4 v[122:125], v[172:179], v[18:25], v[122:125], v234, v235 op_sel_hi:[0,0,0]
	v_mfma_scale_f32_16x16x128_f8f6f4 v[118:121], v[26:33], v[198:205], v[118:121], v234, v235 op_sel_hi:[0,0,0]
	v_mfma_scale_f32_16x16x128_f8f6f4 v[114:117], v[172:179], v[198:205], v[114:117], v234, v235 op_sel_hi:[0,0,0]
	v_mfma_scale_f32_16x16x128_f8f6f4 v[110:113], v[26:33], v[206:213], v[110:113], v234, v235 op_sel_hi:[0,0,0]
	v_mfma_scale_f32_16x16x128_f8f6f4 v[106:109], v[172:179], v[206:213], v[106:109], v234, v235 op_sel_hi:[0,0,0]
	v_mfma_scale_f32_16x16x128_f8f6f4 v[102:105], v[26:33], v[216:223], v[102:105], v234, v235 op_sel_hi:[0,0,0]
	v_mfma_scale_f32_16x16x128_f8f6f4 v[98:101], v[172:179], v[216:223], v[98:101], v234, v235 op_sel_hi:[0,0,0]
	s_setprio 0
	s_barrier
	s_mov_b32 m0, s58
	v_lshl_add_u64 v[18:19], s[44:45], 0, v[0:1]
	s_add_u32 vcc_lo, s44, 0x20000
	ds_read_b128 v[198:201], v196 offset:16384
	ds_read_b128 v[202:205], v196 offset:17408
	ds_read_b128 v[206:209], v196 offset:18432
	ds_read_b128 v[210:213], v196 offset:19456
	ds_read_b128 v[216:219], v196 offset:20480
	ds_read_b128 v[220:223], v196 offset:21504
	ds_read_b128 v[224:227], v196 offset:22528
	ds_read_b128 v[228:231], v196 offset:23552
	global_load_lds_dwordx4 v[18:19], off
	v_lshl_add_u64 v[20:21], s[44:45], 0, v[166:167]
	s_mov_b32 m0, s59
	s_addc_u32 vcc_hi, s45, 0
	global_load_lds_dwordx4 v[20:21], off
	v_lshl_add_u64 v[22:23], vcc, 0, v[0:1]
	s_mov_b32 m0, s60
	v_lshl_add_u64 v[24:25], s[48:49], 0, v[164:165]
	global_load_lds_dwordx4 v[22:23], off
	v_lshl_add_u64 v[22:23], vcc, 0, v[166:167]
	s_mov_b32 m0, s61
	s_nop 0
	global_load_lds_dwordx4 v[22:23], off
	v_lshl_add_u64 v[22:23], s[48:49], 0, v[162:163]
	s_mov_b32 m0, s57
	s_nop 0
	global_load_lds_dwordx4 v[22:23], off
	s_mov_b32 m0, s62
	s_nop 0
	global_load_lds_dwordx4 v[24:25], off
	s_waitcnt vmcnt(8)
	s_waitcnt lgkmcnt(0)
	s_barrier
	s_setprio 1
	s_waitcnt lgkmcnt(0)
	v_mfma_scale_f32_16x16x128_f8f6f4 v[94:97], v[2:9], v[198:205], v[94:97], v234, v235 op_sel_hi:[0,0,0]
	v_mfma_scale_f32_16x16x128_f8f6f4 v[90:93], v[10:17], v[198:205], v[90:93], v234, v235 op_sel_hi:[0,0,0]
	v_mfma_scale_f32_16x16x128_f8f6f4 v[86:89], v[2:9], v[206:213], v[86:89], v234, v235 op_sel_hi:[0,0,0]
	v_mfma_scale_f32_16x16x128_f8f6f4 v[82:85], v[10:17], v[206:213], v[82:85], v234, v235 op_sel_hi:[0,0,0]
	v_mfma_scale_f32_16x16x128_f8f6f4 v[78:81], v[2:9], v[216:223], v[78:81], v234, v235 op_sel_hi:[0,0,0]
	v_mfma_scale_f32_16x16x128_f8f6f4 v[74:77], v[10:17], v[216:223], v[74:77], v234, v235 op_sel_hi:[0,0,0]
	v_mfma_scale_f32_16x16x128_f8f6f4 v[70:73], v[2:9], v[224:231], v[70:73], v234, v235 op_sel_hi:[0,0,0]
	v_mfma_scale_f32_16x16x128_f8f6f4 v[66:69], v[10:17], v[224:231], v[66:69], v234, v235 op_sel_hi:[0,0,0]
	v_mfma_scale_f32_16x16x128_f8f6f4 v[62:65], v[26:33], v[198:205], v[62:65], v234, v235 op_sel_hi:[0,0,0]
	v_mfma_scale_f32_16x16x128_f8f6f4 v[58:61], v[172:179], v[198:205], v[58:61], v234, v235 op_sel_hi:[0,0,0]
	v_mfma_scale_f32_16x16x128_f8f6f4 v[54:57], v[26:33], v[206:213], v[54:57], v234, v235 op_sel_hi:[0,0,0]
	v_mfma_scale_f32_16x16x128_f8f6f4 v[50:53], v[172:179], v[206:213], v[50:53], v234, v235 op_sel_hi:[0,0,0]
	v_mfma_scale_f32_16x16x128_f8f6f4 v[46:49], v[26:33], v[216:223], v[46:49], v234, v235 op_sel_hi:[0,0,0]
	v_mfma_scale_f32_16x16x128_f8f6f4 v[42:45], v[172:179], v[216:223], v[42:45], v234, v235 op_sel_hi:[0,0,0]
	v_mfma_scale_f32_16x16x128_f8f6f4 v[38:41], v[26:33], v[224:231], v[38:41], v234, v235 op_sel_hi:[0,0,0]
	v_mfma_scale_f32_16x16x128_f8f6f4 v[34:37], v[172:179], v[224:231], v[34:37], v234, v235 op_sel_hi:[0,0,0]
	s_setprio 0
	s_barrier
	ds_read_b128 v[10:13], v188
	ds_read_b128 v[14:17], v189
	ds_read_b128 v[26:29], v190
	ds_read_b128 v[30:33], v191
	ds_read_b128 v[2:5], v192
	ds_read_b128 v[6:9], v193
	ds_read_b128 v[172:175], v194
	ds_read_b128 v[176:179], v195
	s_add_u32 s48, s48, 0x20000
	s_addc_u32 s49, s49, 0
	s_mov_b32 m0, s63
	v_lshl_add_u64 v[232:233], s[48:49], 0, v[162:163]
	ds_read_b128 v[198:201], v196 offset:32768
	ds_read_b128 v[202:205], v196 offset:33792
	ds_read_b128 v[206:209], v196 offset:34816
	ds_read_b128 v[210:213], v196 offset:35840
	ds_read_b128 v[216:219], v196 offset:36864
	ds_read_b128 v[220:223], v196 offset:37888
	ds_read_b128 v[224:227], v196 offset:38912
	ds_read_b128 v[228:231], v196 offset:39936
	global_load_lds_dwordx4 v[232:233], off
	v_lshl_add_u64 v[232:233], s[48:49], 0, v[164:165]
	s_mov_b32 m0, s64
	s_nop 0
	global_load_lds_dwordx4 v[232:233], off
	s_waitcnt vmcnt(8)
	s_waitcnt lgkmcnt(0)
	s_barrier
	s_setprio 1
	s_waitcnt lgkmcnt(0)
	v_mfma_scale_f32_16x16x128_f8f6f4 v[158:161], v[10:17], v[198:205], v[158:161], v234, v235 op_sel_hi:[0,0,0]
	v_mfma_scale_f32_16x16x128_f8f6f4 v[154:157], v[26:33], v[198:205], v[154:157], v234, v235 op_sel_hi:[0,0,0]
	v_mfma_scale_f32_16x16x128_f8f6f4 v[150:153], v[10:17], v[206:213], v[150:153], v234, v235 op_sel_hi:[0,0,0]
	v_mfma_scale_f32_16x16x128_f8f6f4 v[146:149], v[26:33], v[206:213], v[146:149], v234, v235 op_sel_hi:[0,0,0]
	v_mfma_scale_f32_16x16x128_f8f6f4 v[142:145], v[10:17], v[216:223], v[142:145], v234, v235 op_sel_hi:[0,0,0]
	v_mfma_scale_f32_16x16x128_f8f6f4 v[138:141], v[26:33], v[216:223], v[138:141], v234, v235 op_sel_hi:[0,0,0]
	v_mfma_scale_f32_16x16x128_f8f6f4 v[134:137], v[10:17], v[224:231], v[134:137], v234, v235 op_sel_hi:[0,0,0]
	v_mfma_scale_f32_16x16x128_f8f6f4 v[130:133], v[26:33], v[224:231], v[130:133], v234, v235 op_sel_hi:[0,0,0]
	v_mfma_scale_f32_16x16x128_f8f6f4 v[126:129], v[2:9], v[198:205], v[126:129], v234, v235 op_sel_hi:[0,0,0]
	v_mfma_scale_f32_16x16x128_f8f6f4 v[122:125], v[172:179], v[198:205], v[122:125], v234, v235 op_sel_hi:[0,0,0]
	v_mfma_scale_f32_16x16x128_f8f6f4 v[118:121], v[2:9], v[206:213], v[118:121], v234, v235 op_sel_hi:[0,0,0]
	v_mfma_scale_f32_16x16x128_f8f6f4 v[114:117], v[172:179], v[206:213], v[114:117], v234, v235 op_sel_hi:[0,0,0]
	v_mfma_scale_f32_16x16x128_f8f6f4 v[110:113], v[2:9], v[216:223], v[110:113], v234, v235 op_sel_hi:[0,0,0]
	v_mfma_scale_f32_16x16x128_f8f6f4 v[106:109], v[172:179], v[216:223], v[106:109], v234, v235 op_sel_hi:[0,0,0]
	v_mfma_scale_f32_16x16x128_f8f6f4 v[102:105], v[2:9], v[224:231], v[102:105], v234, v235 op_sel_hi:[0,0,0]
	v_mfma_scale_f32_16x16x128_f8f6f4 v[98:101], v[172:179], v[224:231], v[98:101], v234, v235 op_sel_hi:[0,0,0]
	s_setprio 0
	s_barrier
	s_mov_b32 m0, s7
	v_lshl_add_u64 v[18:19], v[18:19], 0, s[66:67]
	s_add_u32 s44, s44, 0x20080
	ds_read_b128 v[198:201], v196 offset:49152
	ds_read_b128 v[202:205], v196 offset:50176
	ds_read_b128 v[206:209], v196 offset:51200
	ds_read_b128 v[210:213], v196 offset:52224
	ds_read_b128 v[216:219], v196 offset:53248
	ds_read_b128 v[220:223], v196 offset:54272
	ds_read_b128 v[224:227], v196 offset:55296
	ds_read_b128 v[228:231], v196 offset:56320
	global_load_lds_dwordx4 v[18:19], off
	v_lshl_add_u64 v[18:19], v[20:21], 0, s[66:67]
	s_mov_b32 m0, s65
	s_addc_u32 s45, s45, 0
	global_load_lds_dwordx4 v[18:19], off
	v_lshl_add_u64 v[18:19], s[44:45], 0, v[0:1]
	s_mov_b32 m0, s13
	s_nop 0
	global_load_lds_dwordx4 v[18:19], off
	v_lshl_add_u64 v[18:19], s[44:45], 0, v[166:167]
	s_mov_b32 m0, s51
	s_nop 0
	global_load_lds_dwordx4 v[18:19], off
	v_lshl_add_u64 v[18:19], v[22:23], 0, s[66:67]
	s_mov_b32 m0, s68
	s_nop 0
	global_load_lds_dwordx4 v[18:19], off
	v_lshl_add_u64 v[18:19], v[24:25], 0, s[66:67]
	s_mov_b32 m0, s52
	s_nop 0
	global_load_lds_dwordx4 v[18:19], off
	s_waitcnt vmcnt(8)
	s_waitcnt lgkmcnt(0)
	s_barrier
	s_setprio 1
	s_waitcnt lgkmcnt(0)
	v_mfma_scale_f32_16x16x128_f8f6f4 v[94:97], v[10:17], v[198:205], v[94:97], v234, v235 op_sel_hi:[0,0,0]
	v_mfma_scale_f32_16x16x128_f8f6f4 v[90:93], v[26:33], v[198:205], v[90:93], v234, v235 op_sel_hi:[0,0,0]
	v_mfma_scale_f32_16x16x128_f8f6f4 v[86:89], v[10:17], v[206:213], v[86:89], v234, v235 op_sel_hi:[0,0,0]
	v_mfma_scale_f32_16x16x128_f8f6f4 v[82:85], v[26:33], v[206:213], v[82:85], v234, v235 op_sel_hi:[0,0,0]
	v_mfma_scale_f32_16x16x128_f8f6f4 v[78:81], v[10:17], v[216:223], v[78:81], v234, v235 op_sel_hi:[0,0,0]
	v_mfma_scale_f32_16x16x128_f8f6f4 v[74:77], v[26:33], v[216:223], v[74:77], v234, v235 op_sel_hi:[0,0,0]
	v_mfma_scale_f32_16x16x128_f8f6f4 v[70:73], v[10:17], v[224:231], v[70:73], v234, v235 op_sel_hi:[0,0,0]
	v_mfma_scale_f32_16x16x128_f8f6f4 v[66:69], v[26:33], v[224:231], v[66:69], v234, v235 op_sel_hi:[0,0,0]
	v_mfma_scale_f32_16x16x128_f8f6f4 v[62:65], v[2:9], v[198:205], v[62:65], v234, v235 op_sel_hi:[0,0,0]
	v_mfma_scale_f32_16x16x128_f8f6f4 v[58:61], v[172:179], v[198:205], v[58:61], v234, v235 op_sel_hi:[0,0,0]
	v_mfma_scale_f32_16x16x128_f8f6f4 v[54:57], v[2:9], v[206:213], v[54:57], v234, v235 op_sel_hi:[0,0,0]
	v_mfma_scale_f32_16x16x128_f8f6f4 v[50:53], v[172:179], v[206:213], v[50:53], v234, v235 op_sel_hi:[0,0,0]
	v_mfma_scale_f32_16x16x128_f8f6f4 v[46:49], v[2:9], v[216:223], v[46:49], v234, v235 op_sel_hi:[0,0,0]
	v_mfma_scale_f32_16x16x128_f8f6f4 v[42:45], v[172:179], v[216:223], v[42:45], v234, v235 op_sel_hi:[0,0,0]
	v_mfma_scale_f32_16x16x128_f8f6f4 v[38:41], v[2:9], v[224:231], v[38:41], v234, v235 op_sel_hi:[0,0,0]
	v_mfma_scale_f32_16x16x128_f8f6f4 v[34:37], v[172:179], v[224:231], v[34:37], v234, v235 op_sel_hi:[0,0,0]
	s_setprio 0
	s_barrier
	s_add_i32 s75, s75, 2
	s_add_u32 s46, s46, 0x100
	s_addc_u32 s47, s47, 0
	s_add_u32 s37, s37, 0x100
	s_addc_u32 s74, s74, 0
	s_cmp_gt_u32 s75, 5
	s_cbranch_scc0 .LBB0_388
	s_and_b64 vcc, exec, s[30:31]
	s_cbranch_vccz .LBB0_391
	s_barrier

.LBB0_1368:
	v_add_u32_e32 v134, 0x10000, v226
	v_add_u32_e32 v146, 0x14000, v226
	ds_read_b128 v[150:153], v134
	ds_read_b128 v[154:157], v134 offset:1024
	ds_read_b128 v[158:161], v134 offset:2048
	ds_read_b128 v[162:165], v134 offset:3072
	s_waitcnt vmcnt(0)
	ds_read_b128 v[134:137], v146
	ds_read_b128 v[138:141], v146 offset:1024
	ds_read_b128 v[142:145], v146 offset:2048
	ds_read_b128 v[146:149], v146 offset:3072
	v_lshl_add_u64 v[208:209], s[44:45], 0, v[204:205]
	s_add_i32 m0, s52, 0xc000
	s_waitcnt lgkmcnt(0)
	ds_read_b128 v[178:181], v227
	ds_read_b128 v[194:197], v227 offset:1024
	ds_read_b128 v[174:177], v227 offset:2048
	ds_read_b128 v[190:193], v227 offset:3072
	ds_read_b128 v[170:173], v227 offset:4096
	ds_read_b128 v[186:189], v227 offset:5120
	ds_read_b128 v[166:169], v227 offset:6144
	ds_read_b128 v[182:185], v227 offset:7168
	global_load_lds_dwordx4 v[208:209], off
	v_lshl_add_u64 v[208:209], s[44:45], 0, v[206:207]
	s_add_i32 m0, s52, 0xe000
	s_nop 0
	global_load_lds_dwordx4 v[208:209], off
	s_waitcnt vmcnt(8)
	s_waitcnt lgkmcnt(0)
	s_barrier
	s_setprio 1
	s_waitcnt lgkmcnt(0)
	v_mfma_f32_16x16x32_bf16 v[130:133], v[150:153], v[178:181], v[130:133]
	v_mfma_f32_16x16x32_bf16 v[126:129], v[158:161], v[178:181], v[126:129]
	v_mfma_f32_16x16x32_bf16 v[122:125], v[150:153], v[174:177], v[122:125]
	v_mfma_f32_16x16x32_bf16 v[118:121], v[158:161], v[174:177], v[118:121]
	v_mfma_f32_16x16x32_bf16 v[114:117], v[150:153], v[170:173], v[114:117]
	v_mfma_f32_16x16x32_bf16 v[110:113], v[158:161], v[170:173], v[110:113]
	v_mfma_f32_16x16x32_bf16 v[106:109], v[150:153], v[166:169], v[106:109]
	v_mfma_f32_16x16x32_bf16 v[102:105], v[158:161], v[166:169], v[102:105]
	v_mfma_f32_16x16x32_bf16 v[130:133], v[154:157], v[194:197], v[130:133]
	v_mfma_f32_16x16x32_bf16 v[126:129], v[162:165], v[194:197], v[126:129]
	v_mfma_f32_16x16x32_bf16 v[122:125], v[154:157], v[190:193], v[122:125]
	v_mfma_f32_16x16x32_bf16 v[118:121], v[162:165], v[190:193], v[118:121]
	v_mfma_f32_16x16x32_bf16 v[114:117], v[154:157], v[186:189], v[114:117]
	v_mfma_f32_16x16x32_bf16 v[110:113], v[162:165], v[186:189], v[110:113]
	v_mfma_f32_16x16x32_bf16 v[106:109], v[154:157], v[182:185], v[106:109]
	v_mfma_f32_16x16x32_bf16 v[102:105], v[162:165], v[182:185], v[102:105]
	v_mfma_f32_16x16x32_bf16 v[98:101], v[134:137], v[178:181], v[98:101]
	v_mfma_f32_16x16x32_bf16 v[94:97], v[142:145], v[178:181], v[94:97]
	v_mfma_f32_16x16x32_bf16 v[90:93], v[134:137], v[174:177], v[90:93]
	v_mfma_f32_16x16x32_bf16 v[86:89], v[142:145], v[174:177], v[86:89]
	v_mfma_f32_16x16x32_bf16 v[82:85], v[134:137], v[170:173], v[82:85]
	v_mfma_f32_16x16x32_bf16 v[78:81], v[142:145], v[170:173], v[78:81]
	v_mfma_f32_16x16x32_bf16 v[74:77], v[134:137], v[166:169], v[74:77]
	v_mfma_f32_16x16x32_bf16 v[70:73], v[142:145], v[166:169], v[70:73]
	v_mfma_f32_16x16x32_bf16 v[98:101], v[138:141], v[194:197], v[98:101]
	v_mfma_f32_16x16x32_bf16 v[94:97], v[146:149], v[194:197], v[94:97]
	v_mfma_f32_16x16x32_bf16 v[90:93], v[138:141], v[190:193], v[90:93]
	v_mfma_f32_16x16x32_bf16 v[86:89], v[146:149], v[190:193], v[86:89]
	v_mfma_f32_16x16x32_bf16 v[82:85], v[138:141], v[186:189], v[82:85]
	v_mfma_f32_16x16x32_bf16 v[78:81], v[146:149], v[186:189], v[78:81]
	v_mfma_f32_16x16x32_bf16 v[74:77], v[138:141], v[182:185], v[74:77]
	v_mfma_f32_16x16x32_bf16 v[70:73], v[146:149], v[182:185], v[70:73]
	s_setprio 0
	s_barrier
	v_cndmask_b32_e64 v208, 0, 1, s[6:7]
	v_cmp_ne_u32_e64 s[8:9], 1, v208
	s_andn2_b64 vcc, exec, s[6:7]
	s_cbranch_vccnz .LBB0_1370
	ds_read_b128 v[178:181], v227 offset:16384
	ds_read_b128 v[194:197], v227 offset:17408
	ds_read_b128 v[174:177], v227 offset:18432
	ds_read_b128 v[190:193], v227 offset:19456
	ds_read_b128 v[170:173], v227 offset:20480
	ds_read_b128 v[186:189], v227 offset:21504
	ds_read_b128 v[166:169], v227 offset:22528
	ds_read_b128 v[182:185], v227 offset:23552
.LBB0_1370:
	s_add_u32 s46, s44, 0xfffa0080
	s_addc_u32 s47, s45, -1
	s_cmp_eq_u32 s83, 4
	s_cselect_b32 s49, s41, s47
	s_cselect_b32 s48, s40, s46
	s_cselect_b32 s47, s27, s75
	s_cselect_b32 s46, s39, s74
	s_mov_b32 m0, s53
	v_lshl_add_u64 v[208:209], s[46:47], 0, v[0:1]
	s_add_u32 vcc_lo, s46, 0x20000
	global_load_lds_dwordx4 v[208:209], off
	v_lshl_add_u64 v[210:211], s[46:47], 0, v[202:203]
	s_mov_b32 m0, s54
	s_addc_u32 vcc_hi, s47, 0
	global_load_lds_dwordx4 v[210:211], off
	v_lshl_add_u64 v[212:213], vcc, 0, v[0:1]
	s_mov_b32 m0, s55
	v_lshl_add_u64 v[216:217], s[48:49], 0, v[200:201]
	global_load_lds_dwordx4 v[212:213], off
	v_lshl_add_u64 v[212:213], vcc, 0, v[202:203]
	s_mov_b32 m0, s56
	s_and_b64 vcc, exec, s[8:9]
	global_load_lds_dwordx4 v[212:213], off
	v_lshl_add_u64 v[212:213], s[48:49], 0, v[198:199]
	s_mov_b32 m0, s52
	s_nop 0
	global_load_lds_dwordx4 v[212:213], off
	s_mov_b32 m0, s57
	s_nop 0
	global_load_lds_dwordx4 v[216:217], off
	s_waitcnt vmcnt(8)
	s_waitcnt lgkmcnt(0)
	s_barrier
	s_cbranch_vccnz .LBB0_1372
	s_setprio 1
	s_waitcnt lgkmcnt(0)
	v_mfma_f32_16x16x32_bf16 v[66:69], v[150:153], v[178:181], v[66:69]
	v_mfma_f32_16x16x32_bf16 v[62:65], v[158:161], v[178:181], v[62:65]
	v_mfma_f32_16x16x32_bf16 v[58:61], v[150:153], v[174:177], v[58:61]
	v_mfma_f32_16x16x32_bf16 v[54:57], v[158:161], v[174:177], v[54:57]
	v_mfma_f32_16x16x32_bf16 v[50:53], v[150:153], v[170:173], v[50:53]
	v_mfma_f32_16x16x32_bf16 v[46:49], v[158:161], v[170:173], v[46:49]
	v_mfma_f32_16x16x32_bf16 v[42:45], v[150:153], v[166:169], v[42:45]
	v_mfma_f32_16x16x32_bf16 v[38:41], v[158:161], v[166:169], v[38:41]
	v_mfma_f32_16x16x32_bf16 v[66:69], v[154:157], v[194:197], v[66:69]
	v_mfma_f32_16x16x32_bf16 v[62:65], v[162:165], v[194:197], v[62:65]
	v_mfma_f32_16x16x32_bf16 v[58:61], v[154:157], v[190:193], v[58:61]
	v_mfma_f32_16x16x32_bf16 v[54:57], v[162:165], v[190:193], v[54:57]
	v_mfma_f32_16x16x32_bf16 v[50:53], v[154:157], v[186:189], v[50:53]
	v_mfma_f32_16x16x32_bf16 v[46:49], v[162:165], v[186:189], v[46:49]
	v_mfma_f32_16x16x32_bf16 v[42:45], v[154:157], v[182:185], v[42:45]
	v_mfma_f32_16x16x32_bf16 v[38:41], v[162:165], v[182:185], v[38:41]
	v_mfma_f32_16x16x32_bf16 v[34:37], v[134:137], v[178:181], v[34:37]
	v_mfma_f32_16x16x32_bf16 v[30:33], v[142:145], v[178:181], v[30:33]
	v_mfma_f32_16x16x32_bf16 v[26:29], v[134:137], v[174:177], v[26:29]
	v_mfma_f32_16x16x32_bf16 v[22:25], v[142:145], v[174:177], v[22:25]
	v_mfma_f32_16x16x32_bf16 v[18:21], v[134:137], v[170:173], v[18:21]
	v_mfma_f32_16x16x32_bf16 v[14:17], v[142:145], v[170:173], v[14:17]
	v_mfma_f32_16x16x32_bf16 v[10:13], v[134:137], v[166:169], v[10:13]
	v_mfma_f32_16x16x32_bf16 v[6:9], v[142:145], v[166:169], v[6:9]
	v_mfma_f32_16x16x32_bf16 v[34:37], v[138:141], v[194:197], v[34:37]
	v_mfma_f32_16x16x32_bf16 v[30:33], v[146:149], v[194:197], v[30:33]
	v_mfma_f32_16x16x32_bf16 v[26:29], v[138:141], v[190:193], v[26:29]
	v_mfma_f32_16x16x32_bf16 v[22:25], v[146:149], v[190:193], v[22:25]
	v_mfma_f32_16x16x32_bf16 v[18:21], v[138:141], v[186:189], v[18:21]
	v_mfma_f32_16x16x32_bf16 v[14:17], v[146:149], v[186:189], v[14:17]
	v_mfma_f32_16x16x32_bf16 v[10:13], v[138:141], v[182:185], v[10:13]
	v_mfma_f32_16x16x32_bf16 v[6:9], v[146:149], v[182:185], v[6:9]
	s_setprio 0
.LBB0_1372:
	s_barrier
	v_add_u32_e32 v134, 0x18000, v226
	v_add_u32_e32 v146, 0x1c000, v226
	ds_read_b128 v[150:153], v134
	ds_read_b128 v[154:157], v134 offset:1024
	ds_read_b128 v[158:161], v134 offset:2048
	ds_read_b128 v[162:165], v134 offset:3072
	ds_read_b128 v[134:137], v146
	ds_read_b128 v[138:141], v146 offset:1024
	ds_read_b128 v[142:145], v146 offset:2048
	ds_read_b128 v[146:149], v146 offset:3072
	s_add_u32 s48, s48, 0x60000
	s_addc_u32 s49, s49, 0
	s_mov_b32 m0, s58
	v_lshl_add_u64 v[218:219], s[48:49], 0, v[198:199]
	s_waitcnt lgkmcnt(0)
	ds_read_b128 v[178:181], v227 offset:32768
	ds_read_b128 v[194:197], v227 offset:33792
	ds_read_b128 v[174:177], v227 offset:34816
	ds_read_b128 v[190:193], v227 offset:35840
	ds_read_b128 v[170:173], v227 offset:36864
	ds_read_b128 v[186:189], v227 offset:37888
	ds_read_b128 v[166:169], v227 offset:38912
	ds_read_b128 v[182:185], v227 offset:39936
	global_load_lds_dwordx4 v[218:219], off
	v_lshl_add_u64 v[218:219], s[48:49], 0, v[200:201]
	s_mov_b32 m0, s59
	s_nop 0
	global_load_lds_dwordx4 v[218:219], off
	s_waitcnt vmcnt(8)
	s_waitcnt lgkmcnt(0)
	s_barrier
	s_setprio 1
	s_waitcnt lgkmcnt(0)
	v_mfma_f32_16x16x32_bf16 v[130:133], v[150:153], v[178:181], v[130:133]
	v_mfma_f32_16x16x32_bf16 v[126:129], v[158:161], v[178:181], v[126:129]
	v_mfma_f32_16x16x32_bf16 v[122:125], v[150:153], v[174:177], v[122:125]
	v_mfma_f32_16x16x32_bf16 v[118:121], v[158:161], v[174:177], v[118:121]
	v_mfma_f32_16x16x32_bf16 v[114:117], v[150:153], v[170:173], v[114:117]
	v_mfma_f32_16x16x32_bf16 v[110:113], v[158:161], v[170:173], v[110:113]
	v_mfma_f32_16x16x32_bf16 v[106:109], v[150:153], v[166:169], v[106:109]
	v_mfma_f32_16x16x32_bf16 v[102:105], v[158:161], v[166:169], v[102:105]
	v_mfma_f32_16x16x32_bf16 v[130:133], v[154:157], v[194:197], v[130:133]
	v_mfma_f32_16x16x32_bf16 v[126:129], v[162:165], v[194:197], v[126:129]
	v_mfma_f32_16x16x32_bf16 v[122:125], v[154:157], v[190:193], v[122:125]
	v_mfma_f32_16x16x32_bf16 v[118:121], v[162:165], v[190:193], v[118:121]
	v_mfma_f32_16x16x32_bf16 v[114:117], v[154:157], v[186:189], v[114:117]
	v_mfma_f32_16x16x32_bf16 v[110:113], v[162:165], v[186:189], v[110:113]
	v_mfma_f32_16x16x32_bf16 v[106:109], v[154:157], v[182:185], v[106:109]
	v_mfma_f32_16x16x32_bf16 v[102:105], v[162:165], v[182:185], v[102:105]
	v_mfma_f32_16x16x32_bf16 v[98:101], v[134:137], v[178:181], v[98:101]
	v_mfma_f32_16x16x32_bf16 v[94:97], v[142:145], v[178:181], v[94:97]
	v_mfma_f32_16x16x32_bf16 v[90:93], v[134:137], v[174:177], v[90:93]
	v_mfma_f32_16x16x32_bf16 v[86:89], v[142:145], v[174:177], v[86:89]
	v_mfma_f32_16x16x32_bf16 v[82:85], v[134:137], v[170:173], v[82:85]
	v_mfma_f32_16x16x32_bf16 v[78:81], v[142:145], v[170:173], v[78:81]
	v_mfma_f32_16x16x32_bf16 v[74:77], v[134:137], v[166:169], v[74:77]
	v_mfma_f32_16x16x32_bf16 v[70:73], v[142:145], v[166:169], v[70:73]
	v_mfma_f32_16x16x32_bf16 v[98:101], v[138:141], v[194:197], v[98:101]
	v_mfma_f32_16x16x32_bf16 v[94:97], v[146:149], v[194:197], v[94:97]
	v_mfma_f32_16x16x32_bf16 v[90:93], v[138:141], v[190:193], v[90:93]
	v_mfma_f32_16x16x32_bf16 v[86:89], v[146:149], v[190:193], v[86:89]
	v_mfma_f32_16x16x32_bf16 v[82:85], v[138:141], v[186:189], v[82:85]
	v_mfma_f32_16x16x32_bf16 v[78:81], v[146:149], v[186:189], v[78:81]
	v_mfma_f32_16x16x32_bf16 v[74:77], v[138:141], v[182:185], v[74:77]
	v_mfma_f32_16x16x32_bf16 v[70:73], v[146:149], v[182:185], v[70:73]
	s_setprio 0
	s_barrier
	s_and_b64 vcc, exec, s[8:9]
	s_cbranch_vccnz .LBB0_1374
	ds_read_b128 v[178:181], v227 offset:49152
	ds_read_b128 v[194:197], v227 offset:50176
	ds_read_b128 v[174:177], v227 offset:51200
	ds_read_b128 v[190:193], v227 offset:52224
	ds_read_b128 v[170:173], v227 offset:53248
	ds_read_b128 v[186:189], v227 offset:54272
	ds_read_b128 v[166:169], v227 offset:55296
	ds_read_b128 v[182:185], v227 offset:56320
.LBB0_1374:
	s_mov_b32 m0, s62
	v_lshl_add_u64 v[208:209], v[208:209], 0, s[66:67]
	s_add_u32 s46, s46, 0x20080
	global_load_lds_dwordx4 v[208:209], off
	v_lshl_add_u64 v[208:209], v[210:211], 0, s[66:67]
	s_mov_b32 m0, s63
	s_addc_u32 s47, s47, 0
	global_load_lds_dwordx4 v[208:209], off
	v_lshl_add_u64 v[208:209], s[46:47], 0, v[0:1]
	s_mov_b32 m0, s68
	s_and_b64 vcc, exec, s[8:9]
	global_load_lds_dwordx4 v[208:209], off
	v_lshl_add_u64 v[208:209], s[46:47], 0, v[202:203]
	s_mov_b32 m0, s81
	s_nop 0
	global_load_lds_dwordx4 v[208:209], off
	v_lshl_add_u64 v[208:209], v[212:213], 0, s[66:67]
	s_mov_b32 m0, s64
	s_nop 0
	global_load_lds_dwordx4 v[208:209], off
	v_lshl_add_u64 v[208:209], v[216:217], 0, s[66:67]
	s_mov_b32 m0, s65
	s_nop 0
	global_load_lds_dwordx4 v[208:209], off
	s_waitcnt vmcnt(8)
	s_waitcnt lgkmcnt(0)
	s_barrier
	s_cbranch_vccnz .LBB0_1367
	s_setprio 1
	s_waitcnt lgkmcnt(0)
	v_mfma_f32_16x16x32_bf16 v[66:69], v[150:153], v[178:181], v[66:69]
	v_mfma_f32_16x16x32_bf16 v[62:65], v[158:161], v[178:181], v[62:65]
	v_mfma_f32_16x16x32_bf16 v[58:61], v[150:153], v[174:177], v[58:61]
	v_mfma_f32_16x16x32_bf16 v[54:57], v[158:161], v[174:177], v[54:57]
	v_mfma_f32_16x16x32_bf16 v[50:53], v[150:153], v[170:173], v[50:53]
	v_mfma_f32_16x16x32_bf16 v[46:49], v[158:161], v[170:173], v[46:49]
	v_mfma_f32_16x16x32_bf16 v[42:45], v[150:153], v[166:169], v[42:45]
	v_mfma_f32_16x16x32_bf16 v[38:41], v[158:161], v[166:169], v[38:41]
	v_mfma_f32_16x16x32_bf16 v[66:69], v[154:157], v[194:197], v[66:69]
	v_mfma_f32_16x16x32_bf16 v[62:65], v[162:165], v[194:197], v[62:65]
	v_mfma_f32_16x16x32_bf16 v[58:61], v[154:157], v[190:193], v[58:61]
	v_mfma_f32_16x16x32_bf16 v[54:57], v[162:165], v[190:193], v[54:57]
	v_mfma_f32_16x16x32_bf16 v[50:53], v[154:157], v[186:189], v[50:53]
	v_mfma_f32_16x16x32_bf16 v[46:49], v[162:165], v[186:189], v[46:49]
	v_mfma_f32_16x16x32_bf16 v[42:45], v[154:157], v[182:185], v[42:45]
	v_mfma_f32_16x16x32_bf16 v[38:41], v[162:165], v[182:185], v[38:41]
	v_mfma_f32_16x16x32_bf16 v[34:37], v[134:137], v[178:181], v[34:37]
	v_mfma_f32_16x16x32_bf16 v[30:33], v[142:145], v[178:181], v[30:33]
	v_mfma_f32_16x16x32_bf16 v[26:29], v[134:137], v[174:177], v[26:29]
	v_mfma_f32_16x16x32_bf16 v[22:25], v[142:145], v[174:177], v[22:25]
	v_mfma_f32_16x16x32_bf16 v[18:21], v[134:137], v[170:173], v[18:21]
	v_mfma_f32_16x16x32_bf16 v[14:17], v[142:145], v[170:173], v[14:17]
	v_mfma_f32_16x16x32_bf16 v[10:13], v[134:137], v[166:169], v[10:13]
	v_mfma_f32_16x16x32_bf16 v[6:9], v[142:145], v[166:169], v[6:9]
	v_mfma_f32_16x16x32_bf16 v[34:37], v[138:141], v[194:197], v[34:37]
	v_mfma_f32_16x16x32_bf16 v[30:33], v[146:149], v[194:197], v[30:33]
	v_mfma_f32_16x16x32_bf16 v[26:29], v[138:141], v[190:193], v[26:29]
	v_mfma_f32_16x16x32_bf16 v[22:25], v[146:149], v[190:193], v[22:25]
	v_mfma_f32_16x16x32_bf16 v[18:21], v[138:141], v[186:189], v[18:21]
	v_mfma_f32_16x16x32_bf16 v[14:17], v[146:149], v[186:189], v[14:17]
	v_mfma_f32_16x16x32_bf16 v[10:13], v[138:141], v[182:185], v[10:13]
	v_mfma_f32_16x16x32_bf16 v[6:9], v[146:149], v[182:185], v[6:9]
	s_setprio 0
	s_branch .LBB0_1367

.LBB0_1556:
	v_add_u32_e32 v54, 0x10000, v247
	ds_read_b128 v[166:169], v54
	ds_read_b128 v[170:173], v54 offset:1024
	ds_read_b128 v[174:177], v54 offset:2048
	ds_read_b128 v[178:181], v54 offset:3072
	v_add_u32_e32 v54, 0x14000, v247
	ds_read_b128 v[150:153], v54
	ds_read_b128 v[154:157], v54 offset:1024
	ds_read_b128 v[158:161], v54 offset:2048
	ds_read_b128 v[162:165], v54 offset:3072
	v_lshl_add_u64 v[54:55], s[40:41], 0, v[222:223]
	s_add_i32 m0, s26, 0xc000
	s_waitcnt lgkmcnt(0)
	ds_read_b128 v[194:197], v248
	ds_read_b128 v[210:213], v248 offset:1024
	ds_read_b128 v[190:193], v248 offset:2048
	ds_read_b128 v[206:209], v248 offset:3072
	ds_read_b128 v[186:189], v248 offset:4096
	ds_read_b128 v[202:205], v248 offset:5120
	ds_read_b128 v[182:185], v248 offset:6144
	ds_read_b128 v[198:201], v248 offset:7168
	global_load_lds_dwordx4 v[54:55], off
	v_lshl_add_u64 v[54:55], s[40:41], 0, v[224:225]
	s_add_i32 m0, s26, 0xe000
	s_nop 0
	global_load_lds_dwordx4 v[54:55], off
	s_waitcnt vmcnt(8)
	s_waitcnt lgkmcnt(0)
	s_barrier
	s_setprio 1
	s_waitcnt lgkmcnt(0)
	v_mfma_f32_16x16x32_bf16 v[54:57], v[166:169], v[194:197], v[146:149]
	v_mfma_f32_16x16x32_bf16 v[58:61], v[174:177], v[194:197], v[142:145]
	v_mfma_f32_16x16x32_bf16 v[66:69], v[166:169], v[190:193], v[130:133]
	v_mfma_f32_16x16x32_bf16 v[74:77], v[174:177], v[190:193], v[126:129]
	v_mfma_f32_16x16x32_bf16 v[114:117], v[166:169], v[186:189], v[114:117]
	v_mfma_f32_16x16x32_bf16 v[110:113], v[174:177], v[186:189], v[110:113]
	v_mfma_f32_16x16x32_bf16 v[98:101], v[166:169], v[182:185], v[98:101]
	v_mfma_f32_16x16x32_bf16 v[94:97], v[174:177], v[182:185], v[94:97]
	v_mfma_f32_16x16x32_bf16 v[54:57], v[170:173], v[210:213], v[54:57]
	v_mfma_f32_16x16x32_bf16 v[58:61], v[178:181], v[210:213], v[58:61]
	v_mfma_f32_16x16x32_bf16 v[66:69], v[170:173], v[206:209], v[66:69]
	v_mfma_f32_16x16x32_bf16 v[74:77], v[178:181], v[206:209], v[74:77]
	v_mfma_f32_16x16x32_bf16 v[114:117], v[170:173], v[202:205], v[114:117]
	v_mfma_f32_16x16x32_bf16 v[110:113], v[178:181], v[202:205], v[110:113]
	v_mfma_f32_16x16x32_bf16 v[98:101], v[170:173], v[198:201], v[98:101]
	v_mfma_f32_16x16x32_bf16 v[94:97], v[178:181], v[198:201], v[94:97]
	v_mfma_f32_16x16x32_bf16 v[126:129], v[150:153], v[194:197], v[138:141]
	v_mfma_f32_16x16x32_bf16 v[138:141], v[154:157], v[210:213], v[126:129]
	v_mfma_f32_16x16x32_bf16 v[126:129], v[158:161], v[194:197], v[134:137]
	v_mfma_f32_16x16x32_bf16 v[122:125], v[150:153], v[190:193], v[122:125]
	v_mfma_f32_16x16x32_bf16 v[118:121], v[158:161], v[190:193], v[118:121]
	v_mfma_f32_16x16x32_bf16 v[106:109], v[150:153], v[186:189], v[106:109]
	v_mfma_f32_16x16x32_bf16 v[102:105], v[158:161], v[186:189], v[102:105]
	v_mfma_f32_16x16x32_bf16 v[90:93], v[150:153], v[182:185], v[90:93]
	v_mfma_f32_16x16x32_bf16 v[86:89], v[158:161], v[182:185], v[86:89]
	v_mfma_f32_16x16x32_bf16 v[134:137], v[162:165], v[210:213], v[126:129]
	v_mfma_f32_16x16x32_bf16 v[122:125], v[154:157], v[206:209], v[122:125]
	v_mfma_f32_16x16x32_bf16 v[118:121], v[162:165], v[206:209], v[118:121]
	v_mfma_f32_16x16x32_bf16 v[106:109], v[154:157], v[202:205], v[106:109]
	v_mfma_f32_16x16x32_bf16 v[102:105], v[162:165], v[202:205], v[102:105]
	v_mfma_f32_16x16x32_bf16 v[90:93], v[154:157], v[198:201], v[90:93]
	v_mfma_f32_16x16x32_bf16 v[86:89], v[162:165], v[198:201], v[86:89]
	s_setprio 0
	s_barrier
	v_cndmask_b32_e64 v126, 0, 1, s[38:39]
	v_cmp_ne_u32_e64 s[0:1], 1, v126
	s_andn2_b64 vcc, exec, s[38:39]
	s_cbranch_vccnz .LBB0_1558
	ds_read_b128 v[194:197], v248 offset:16384
	ds_read_b128 v[210:213], v248 offset:17408
	ds_read_b128 v[190:193], v248 offset:18432
	ds_read_b128 v[206:209], v248 offset:19456
	ds_read_b128 v[186:189], v248 offset:20480
	ds_read_b128 v[202:205], v248 offset:21504
	ds_read_b128 v[182:185], v248 offset:22528
	ds_read_b128 v[198:201], v248 offset:23552
.LBB0_1558:
	s_add_u32 s42, s40, 0xfffc0080
	s_addc_u32 s43, s41, -1
	s_cmp_eq_u32 s90, 12
	s_cselect_b32 s45, s74, s43
	s_cselect_b32 s44, s75, s42
	s_cselect_b32 s43, s11, s88
	s_cselect_b32 s42, s81, s83
	s_mov_b32 m0, s27
	v_lshl_add_u64 v[226:227], s[42:43], 0, v[0:1]
	s_add_u32 vcc_lo, s42, 0x40000
	global_load_lds_dwordx4 v[226:227], off
	v_lshl_add_u64 v[228:229], s[42:43], 0, v[220:221]
	s_mov_b32 m0, s37
	s_addc_u32 vcc_hi, s43, 0
	global_load_lds_dwordx4 v[228:229], off
	v_lshl_add_u64 v[126:127], vcc, 0, v[0:1]
	s_mov_b32 m0, s47
	v_lshl_add_u64 v[230:231], s[44:45], 0, v[216:217]
	global_load_lds_dwordx4 v[126:127], off
	v_lshl_add_u64 v[126:127], vcc, 0, v[220:221]
	s_mov_b32 m0, s48
	v_lshl_add_u64 v[232:233], s[44:45], 0, v[218:219]
	global_load_lds_dwordx4 v[126:127], off
	s_mov_b32 m0, s26
	s_and_b64 vcc, exec, s[0:1]
	global_load_lds_dwordx4 v[230:231], off
	s_mov_b32 m0, s49
	s_nop 0
	global_load_lds_dwordx4 v[232:233], off
	s_waitcnt vmcnt(8)
	s_waitcnt lgkmcnt(0)
	s_barrier
	s_cbranch_vccnz .LBB0_1560
	s_setprio 1
	s_waitcnt lgkmcnt(0)
	v_mfma_f32_16x16x32_bf16 v[82:85], v[166:169], v[194:197], v[82:85]
	v_mfma_f32_16x16x32_bf16 v[78:81], v[174:177], v[194:197], v[78:81]
	v_mfma_f32_16x16x32_bf16 v[50:53], v[166:169], v[190:193], v[50:53]
	v_mfma_f32_16x16x32_bf16 v[46:49], v[174:177], v[190:193], v[46:49]
	v_mfma_f32_16x16x32_bf16 v[34:37], v[166:169], v[186:189], v[34:37]
	v_mfma_f32_16x16x32_bf16 v[30:33], v[174:177], v[186:189], v[30:33]
	v_mfma_f32_16x16x32_bf16 v[18:21], v[166:169], v[182:185], v[18:21]
	v_mfma_f32_16x16x32_bf16 v[14:17], v[174:177], v[182:185], v[14:17]
	v_mfma_f32_16x16x32_bf16 v[82:85], v[170:173], v[210:213], v[82:85]
	v_mfma_f32_16x16x32_bf16 v[78:81], v[178:181], v[210:213], v[78:81]
	v_mfma_f32_16x16x32_bf16 v[50:53], v[170:173], v[206:209], v[50:53]
	v_mfma_f32_16x16x32_bf16 v[46:49], v[178:181], v[206:209], v[46:49]
	v_mfma_f32_16x16x32_bf16 v[34:37], v[170:173], v[202:205], v[34:37]
	v_mfma_f32_16x16x32_bf16 v[30:33], v[178:181], v[202:205], v[30:33]
	v_mfma_f32_16x16x32_bf16 v[18:21], v[170:173], v[198:201], v[18:21]
	v_mfma_f32_16x16x32_bf16 v[14:17], v[178:181], v[198:201], v[14:17]
	v_mfma_f32_16x16x32_bf16 v[70:73], v[150:153], v[194:197], v[70:73]
	v_mfma_f32_16x16x32_bf16 v[62:65], v[158:161], v[194:197], v[62:65]
	v_mfma_f32_16x16x32_bf16 v[42:45], v[150:153], v[190:193], v[42:45]
	v_mfma_f32_16x16x32_bf16 v[38:41], v[158:161], v[190:193], v[38:41]
	v_mfma_f32_16x16x32_bf16 v[26:29], v[150:153], v[186:189], v[26:29]
	v_mfma_f32_16x16x32_bf16 v[22:25], v[158:161], v[186:189], v[22:25]
	v_mfma_f32_16x16x32_bf16 v[10:13], v[150:153], v[182:185], v[10:13]
	v_mfma_f32_16x16x32_bf16 v[6:9], v[158:161], v[182:185], v[6:9]
	v_mfma_f32_16x16x32_bf16 v[70:73], v[154:157], v[210:213], v[70:73]
	v_mfma_f32_16x16x32_bf16 v[62:65], v[162:165], v[210:213], v[62:65]
	v_mfma_f32_16x16x32_bf16 v[42:45], v[154:157], v[206:209], v[42:45]
	v_mfma_f32_16x16x32_bf16 v[38:41], v[162:165], v[206:209], v[38:41]
	v_mfma_f32_16x16x32_bf16 v[26:29], v[154:157], v[202:205], v[26:29]
	v_mfma_f32_16x16x32_bf16 v[22:25], v[162:165], v[202:205], v[22:25]
	v_mfma_f32_16x16x32_bf16 v[10:13], v[154:157], v[198:201], v[10:13]
	v_mfma_f32_16x16x32_bf16 v[6:9], v[162:165], v[198:201], v[6:9]
	s_setprio 0
.LBB0_1560:
	s_barrier
	v_add_u32_e32 v126, 0x18000, v247
	ds_read_b128 v[166:169], v126
	ds_read_b128 v[170:173], v126 offset:1024
	ds_read_b128 v[174:177], v126 offset:2048
	ds_read_b128 v[178:181], v126 offset:3072
	v_add_u32_e32 v126, 0x1c000, v247
	ds_read_b128 v[150:153], v126
	ds_read_b128 v[154:157], v126 offset:1024
	ds_read_b128 v[158:161], v126 offset:2048
	ds_read_b128 v[162:165], v126 offset:3072
	s_add_u32 s44, s44, 0x40000
	s_addc_u32 s45, s45, 0
	s_mov_b32 m0, s50
	v_lshl_add_u64 v[126:127], s[44:45], 0, v[216:217]
	s_waitcnt lgkmcnt(0)
	ds_read_b128 v[194:197], v248 offset:32768
	ds_read_b128 v[210:213], v248 offset:33792
	ds_read_b128 v[190:193], v248 offset:34816
	ds_read_b128 v[206:209], v248 offset:35840
	ds_read_b128 v[186:189], v248 offset:36864
	ds_read_b128 v[202:205], v248 offset:37888
	ds_read_b128 v[182:185], v248 offset:38912
	ds_read_b128 v[198:201], v248 offset:39936
	global_load_lds_dwordx4 v[126:127], off
	v_lshl_add_u64 v[126:127], s[44:45], 0, v[218:219]
	s_mov_b32 m0, s51
	s_nop 0
	global_load_lds_dwordx4 v[126:127], off
	s_waitcnt vmcnt(8)
	s_waitcnt lgkmcnt(0)
	s_barrier
	s_setprio 1
	s_waitcnt lgkmcnt(0)
	v_mfma_f32_16x16x32_bf16 v[54:57], v[166:169], v[194:197], v[54:57]
	v_mfma_f32_16x16x32_bf16 v[146:149], v[170:173], v[210:213], v[54:57]
	v_mfma_f32_16x16x32_bf16 v[54:57], v[174:177], v[194:197], v[58:61]
	v_mfma_f32_16x16x32_bf16 v[142:145], v[178:181], v[210:213], v[54:57]
	v_mfma_f32_16x16x32_bf16 v[54:57], v[166:169], v[190:193], v[66:69]
	v_mfma_f32_16x16x32_bf16 v[130:133], v[170:173], v[206:209], v[54:57]
	v_mfma_f32_16x16x32_bf16 v[54:57], v[174:177], v[190:193], v[74:77]
	v_mfma_f32_16x16x32_bf16 v[126:129], v[178:181], v[206:209], v[54:57]
	v_mfma_f32_16x16x32_bf16 v[54:57], v[166:169], v[186:189], v[114:117]
	v_mfma_f32_16x16x32_bf16 v[114:117], v[170:173], v[202:205], v[54:57]
	v_mfma_f32_16x16x32_bf16 v[54:57], v[174:177], v[186:189], v[110:113]
	v_mfma_f32_16x16x32_bf16 v[110:113], v[178:181], v[202:205], v[54:57]
	v_mfma_f32_16x16x32_bf16 v[54:57], v[166:169], v[182:185], v[98:101]
	v_mfma_f32_16x16x32_bf16 v[98:101], v[170:173], v[198:201], v[54:57]
	v_mfma_f32_16x16x32_bf16 v[54:57], v[174:177], v[182:185], v[94:97]
	v_mfma_f32_16x16x32_bf16 v[94:97], v[178:181], v[198:201], v[54:57]
	v_mfma_f32_16x16x32_bf16 v[54:57], v[150:153], v[194:197], v[138:141]
	v_mfma_f32_16x16x32_bf16 v[138:141], v[154:157], v[210:213], v[54:57]
	v_mfma_f32_16x16x32_bf16 v[54:57], v[158:161], v[194:197], v[134:137]
	v_mfma_f32_16x16x32_bf16 v[134:137], v[162:165], v[210:213], v[54:57]
	v_mfma_f32_16x16x32_bf16 v[54:57], v[150:153], v[190:193], v[122:125]
	v_mfma_f32_16x16x32_bf16 v[122:125], v[154:157], v[206:209], v[54:57]
	v_mfma_f32_16x16x32_bf16 v[54:57], v[158:161], v[190:193], v[118:121]
	v_mfma_f32_16x16x32_bf16 v[118:121], v[162:165], v[206:209], v[54:57]
	v_mfma_f32_16x16x32_bf16 v[54:57], v[150:153], v[186:189], v[106:109]
	v_mfma_f32_16x16x32_bf16 v[106:109], v[154:157], v[202:205], v[54:57]
	v_mfma_f32_16x16x32_bf16 v[54:57], v[158:161], v[186:189], v[102:105]
	v_mfma_f32_16x16x32_bf16 v[102:105], v[162:165], v[202:205], v[54:57]
	v_mfma_f32_16x16x32_bf16 v[54:57], v[150:153], v[182:185], v[90:93]
	v_mfma_f32_16x16x32_bf16 v[90:93], v[154:157], v[198:201], v[54:57]
	v_mfma_f32_16x16x32_bf16 v[54:57], v[158:161], v[182:185], v[86:89]
	v_mfma_f32_16x16x32_bf16 v[86:89], v[162:165], v[198:201], v[54:57]
	s_setprio 0
	s_barrier
	s_and_b64 vcc, exec, s[0:1]
	s_cbranch_vccnz .LBB0_1562
	ds_read_b128 v[194:197], v248 offset:49152
	ds_read_b128 v[210:213], v248 offset:50176
	ds_read_b128 v[190:193], v248 offset:51200
	ds_read_b128 v[206:209], v248 offset:52224
	ds_read_b128 v[186:189], v248 offset:53248
	ds_read_b128 v[202:205], v248 offset:54272
	ds_read_b128 v[182:185], v248 offset:55296
	ds_read_b128 v[198:201], v248 offset:56320
.LBB0_1562:
	s_mov_b32 m0, s56
	s_nop 1
	v_lshl_add_u64 v[54:55], v[226:227], 0, s[66:67]
	s_add_u32 s42, s42, 0x40080
	global_load_lds_dwordx4 v[54:55], off
	v_lshl_add_u64 v[54:55], v[228:229], 0, s[66:67]
	s_mov_b32 m0, s57
	s_addc_u32 s43, s43, 0
	global_load_lds_dwordx4 v[54:55], off
	v_lshl_add_u64 v[54:55], s[42:43], 0, v[0:1]
	s_mov_b32 m0, s60
	s_and_b64 vcc, exec, s[0:1]
	global_load_lds_dwordx4 v[54:55], off
	v_lshl_add_u64 v[54:55], s[42:43], 0, v[220:221]
	s_mov_b32 m0, s61
	s_nop 0
	global_load_lds_dwordx4 v[54:55], off
	v_lshl_add_u64 v[54:55], v[230:231], 0, s[66:67]
	s_mov_b32 m0, s58
	s_nop 0
	global_load_lds_dwordx4 v[54:55], off
	v_lshl_add_u64 v[54:55], v[232:233], 0, s[66:67]
	s_mov_b32 m0, s59
	s_nop 0
	global_load_lds_dwordx4 v[54:55], off
	s_waitcnt vmcnt(8)
	s_waitcnt lgkmcnt(0)
	s_barrier
	s_cbranch_vccnz .LBB0_1555
	s_setprio 1
	s_waitcnt lgkmcnt(0)
	v_mfma_f32_16x16x32_bf16 v[54:57], v[166:169], v[194:197], v[82:85]
	v_mfma_f32_16x16x32_bf16 v[82:85], v[170:173], v[210:213], v[54:57]
	v_mfma_f32_16x16x32_bf16 v[54:57], v[174:177], v[194:197], v[78:81]
	v_mfma_f32_16x16x32_bf16 v[50:53], v[166:169], v[190:193], v[50:53]
	v_mfma_f32_16x16x32_bf16 v[46:49], v[174:177], v[190:193], v[46:49]
	v_mfma_f32_16x16x32_bf16 v[34:37], v[166:169], v[186:189], v[34:37]
	v_mfma_f32_16x16x32_bf16 v[30:33], v[174:177], v[186:189], v[30:33]
	v_mfma_f32_16x16x32_bf16 v[18:21], v[166:169], v[182:185], v[18:21]
	v_mfma_f32_16x16x32_bf16 v[14:17], v[174:177], v[182:185], v[14:17]
	v_mfma_f32_16x16x32_bf16 v[78:81], v[178:181], v[210:213], v[54:57]
	v_mfma_f32_16x16x32_bf16 v[50:53], v[170:173], v[206:209], v[50:53]
	v_mfma_f32_16x16x32_bf16 v[46:49], v[178:181], v[206:209], v[46:49]
	v_mfma_f32_16x16x32_bf16 v[34:37], v[170:173], v[202:205], v[34:37]
	v_mfma_f32_16x16x32_bf16 v[30:33], v[178:181], v[202:205], v[30:33]
	v_mfma_f32_16x16x32_bf16 v[18:21], v[170:173], v[198:201], v[18:21]
	v_mfma_f32_16x16x32_bf16 v[14:17], v[178:181], v[198:201], v[14:17]
	v_mfma_f32_16x16x32_bf16 v[54:57], v[150:153], v[194:197], v[70:73]
	v_mfma_f32_16x16x32_bf16 v[70:73], v[154:157], v[210:213], v[54:57]
	v_mfma_f32_16x16x32_bf16 v[54:57], v[158:161], v[194:197], v[62:65]
	v_mfma_f32_16x16x32_bf16 v[42:45], v[150:153], v[190:193], v[42:45]
	v_mfma_f32_16x16x32_bf16 v[38:41], v[158:161], v[190:193], v[38:41]
	v_mfma_f32_16x16x32_bf16 v[26:29], v[150:153], v[186:189], v[26:29]
	v_mfma_f32_16x16x32_bf16 v[22:25], v[158:161], v[186:189], v[22:25]
	v_mfma_f32_16x16x32_bf16 v[10:13], v[150:153], v[182:185], v[10:13]
	v_mfma_f32_16x16x32_bf16 v[6:9], v[158:161], v[182:185], v[6:9]
	v_mfma_f32_16x16x32_bf16 v[62:65], v[162:165], v[210:213], v[54:57]
	v_mfma_f32_16x16x32_bf16 v[42:45], v[154:157], v[206:209], v[42:45]
	v_mfma_f32_16x16x32_bf16 v[38:41], v[162:165], v[206:209], v[38:41]
	v_mfma_f32_16x16x32_bf16 v[26:29], v[154:157], v[202:205], v[26:29]
	v_mfma_f32_16x16x32_bf16 v[22:25], v[162:165], v[202:205], v[22:25]
	v_mfma_f32_16x16x32_bf16 v[10:13], v[154:157], v[198:201], v[10:13]
	v_mfma_f32_16x16x32_bf16 v[6:9], v[162:165], v[198:201], v[6:9]
	s_setprio 0
	s_branch .LBB0_1555

.Lrw_done_g1_0:
	s_waitcnt lgkmcnt(0)
	v_mov_b32_e32 v169, v1
	s_barrier
	s_setprio 1
	s_waitcnt lgkmcnt(0)
	v_mfma_scale_f32_16x16x128_f8f6f4 v[150:153], v[26:33], v[198:205], 0, v234, v235 op_sel_hi:[0,0,0]
	v_mfma_scale_f32_16x16x128_f8f6f4 v[146:149], v[18:25], v[198:205], 0, v234, v235 op_sel_hi:[0,0,0]
	v_mfma_scale_f32_16x16x128_f8f6f4 v[142:145], v[26:33], v[206:213], 0, v234, v235 op_sel_hi:[0,0,0]
	v_mfma_scale_f32_16x16x128_f8f6f4 v[138:141], v[18:25], v[206:213], 0, v234, v235 op_sel_hi:[0,0,0]
	v_mfma_scale_f32_16x16x128_f8f6f4 v[134:137], v[26:33], v[216:223], 0, v234, v235 op_sel_hi:[0,0,0]
	v_mfma_scale_f32_16x16x128_f8f6f4 v[130:133], v[18:25], v[216:223], 0, v234, v235 op_sel_hi:[0,0,0]
	v_mfma_scale_f32_16x16x128_f8f6f4 v[126:129], v[26:33], v[224:231], 0, v234, v235 op_sel_hi:[0,0,0]
	v_mfma_scale_f32_16x16x128_f8f6f4 v[122:125], v[18:25], v[224:231], 0, v234, v235 op_sel_hi:[0,0,0]
	v_mfma_scale_f32_16x16x128_f8f6f4 v[118:121], v[10:17], v[198:205], 0, v234, v235 op_sel_hi:[0,0,0]
	v_mfma_scale_f32_16x16x128_f8f6f4 v[114:117], v[2:9], v[198:205], 0, v234, v235 op_sel_hi:[0,0,0]
	v_mfma_scale_f32_16x16x128_f8f6f4 v[110:113], v[10:17], v[206:213], 0, v234, v235 op_sel_hi:[0,0,0]
	v_mfma_scale_f32_16x16x128_f8f6f4 v[106:109], v[2:9], v[206:213], 0, v234, v235 op_sel_hi:[0,0,0]
	v_mfma_scale_f32_16x16x128_f8f6f4 v[102:105], v[10:17], v[216:223], 0, v234, v235 op_sel_hi:[0,0,0]
	v_mfma_scale_f32_16x16x128_f8f6f4 v[98:101], v[2:9], v[216:223], 0, v234, v235 op_sel_hi:[0,0,0]
	v_mfma_scale_f32_16x16x128_f8f6f4 v[94:97], v[10:17], v[224:231], 0, v234, v235 op_sel_hi:[0,0,0]
	v_mfma_scale_f32_16x16x128_f8f6f4 v[90:93], v[2:9], v[224:231], 0, v234, v235 op_sel_hi:[0,0,0]
	s_setprio 0
	s_barrier
	v_lshl_add_u64 v[170:171], s[4:5], 0, v[162:163]
	s_mov_b64 s[54:55], 0x100
	s_mov_b32 m0, s68
	v_lshl_add_u64 v[172:173], v[170:171], 0, s[54:55]
	ds_read_b128 v[198:201], v192 offset:16384
	ds_read_b128 v[202:205], v192 offset:17408
	ds_read_b128 v[206:209], v192 offset:18432
	ds_read_b128 v[210:213], v192 offset:19456
	ds_read_b128 v[216:219], v192 offset:20480
	ds_read_b128 v[220:223], v192 offset:21504
	ds_read_b128 v[224:227], v192 offset:22528
	ds_read_b128 v[228:231], v192 offset:23552
	global_load_lds_dwordx4 v[172:173], off
	v_lshl_add_u64 v[172:173], s[4:5], 0, v[164:165]
	v_lshl_add_u64 v[232:233], v[172:173], 0, s[54:55]
	s_add_u32 s54, s4, 0x20100
	s_mov_b32 m0, s60
	s_addc_u32 s55, s5, 0
	global_load_lds_dwordx4 v[232:233], off
	v_lshl_add_u64 v[232:233], s[54:55], 0, v[162:163]
	s_mov_b32 m0, s61
	v_lshlrev_b32_e32 v0, 10, v195
	global_load_lds_dwordx4 v[232:233], off
	v_lshl_add_u64 v[232:233], s[54:55], 0, v[164:165]
	s_mov_b32 m0, s62
	v_and_or_b32 v0, v0, s82, v174
	global_load_lds_dwordx4 v[232:233], off
	v_bfe_u32 v197, v195, 16, 16
	s_mov_b32 m0, s65
	v_lshl_add_u32 v197, v197, 10, v175
	global_load_lds_dwordx4 v0, s[34:35]
	s_mov_b32 m0, s63
	s_nop 0
	global_load_lds_dwordx4 v197, s[34:35]
	s_cmp_eq_u32 s23, 0
	s_cbranch_scc1 .Lrw_first_g1_1
	s_waitcnt vmcnt(12)
	s_branch .Lrw_done_g1_1

.Lrw_done_g1_1:
	s_waitcnt lgkmcnt(0)
	s_barrier
	s_setprio 1
	s_waitcnt lgkmcnt(0)
	v_mfma_scale_f32_16x16x128_f8f6f4 v[86:89], v[26:33], v[198:205], 0, v234, v235 op_sel_hi:[0,0,0]
	v_mfma_scale_f32_16x16x128_f8f6f4 v[82:85], v[18:25], v[198:205], 0, v234, v235 op_sel_hi:[0,0,0]
	v_mfma_scale_f32_16x16x128_f8f6f4 v[78:81], v[26:33], v[206:213], 0, v234, v235 op_sel_hi:[0,0,0]
	v_mfma_scale_f32_16x16x128_f8f6f4 v[74:77], v[18:25], v[206:213], 0, v234, v235 op_sel_hi:[0,0,0]
	v_mfma_scale_f32_16x16x128_f8f6f4 v[70:73], v[26:33], v[216:223], 0, v234, v235 op_sel_hi:[0,0,0]
	v_mfma_scale_f32_16x16x128_f8f6f4 v[66:69], v[18:25], v[216:223], 0, v234, v235 op_sel_hi:[0,0,0]
	v_mfma_scale_f32_16x16x128_f8f6f4 v[62:65], v[26:33], v[224:231], 0, v234, v235 op_sel_hi:[0,0,0]
	v_mfma_scale_f32_16x16x128_f8f6f4 v[58:61], v[18:25], v[224:231], 0, v234, v235 op_sel_hi:[0,0,0]
	v_mfma_scale_f32_16x16x128_f8f6f4 v[54:57], v[10:17], v[198:205], 0, v234, v235 op_sel_hi:[0,0,0]
	v_mfma_scale_f32_16x16x128_f8f6f4 v[50:53], v[2:9], v[198:205], 0, v234, v235 op_sel_hi:[0,0,0]
	v_mfma_scale_f32_16x16x128_f8f6f4 v[46:49], v[10:17], v[206:213], 0, v234, v235 op_sel_hi:[0,0,0]
	v_mfma_scale_f32_16x16x128_f8f6f4 v[42:45], v[2:9], v[206:213], 0, v234, v235 op_sel_hi:[0,0,0]
	v_mfma_scale_f32_16x16x128_f8f6f4 v[38:41], v[10:17], v[216:223], 0, v234, v235 op_sel_hi:[0,0,0]
	v_mfma_scale_f32_16x16x128_f8f6f4 v[34:37], v[2:9], v[216:223], 0, v234, v235 op_sel_hi:[0,0,0]
	v_mfma_scale_f32_16x16x128_f8f6f4 v[154:157], v[10:17], v[224:231], 0, v234, v235 op_sel_hi:[0,0,0]
	v_mfma_scale_f32_16x16x128_f8f6f4 v[158:161], v[2:9], v[224:231], 0, v234, v235 op_sel_hi:[0,0,0]
	s_setprio 0
	s_barrier
	ds_read_b128 v[18:21], v184
	ds_read_b128 v[22:25], v185
	ds_read_b128 v[26:29], v186
	ds_read_b128 v[30:33], v187
	ds_read_b128 v[2:5], v188
	ds_read_b128 v[6:9], v189
	ds_read_b128 v[10:13], v190
	ds_read_b128 v[14:17], v191
	s_mov_b32 m0, s10
	ds_read_b128 v[198:201], v192 offset:32768
	ds_read_b128 v[202:205], v192 offset:33792
	ds_read_b128 v[206:209], v192 offset:34816
	ds_read_b128 v[210:213], v192 offset:35840
	ds_read_b128 v[216:219], v192 offset:36864
	ds_read_b128 v[220:223], v192 offset:37888
	ds_read_b128 v[224:227], v192 offset:38912
	ds_read_b128 v[228:231], v192 offset:39936
	global_load_lds_dwordx4 v166, s[34:35]
	s_mov_b32 m0, s11
	s_nop 0
	global_load_lds_dwordx4 v168, s[34:35]
	s_waitcnt vmcnt(8)
	s_waitcnt lgkmcnt(0)
	s_barrier
	s_setprio 1
	s_waitcnt lgkmcnt(0)
	v_mfma_scale_f32_16x16x128_f8f6f4 v[150:153], v[18:25], v[198:205], v[150:153], v234, v235 op_sel_hi:[0,0,0]
	v_mfma_scale_f32_16x16x128_f8f6f4 v[146:149], v[26:33], v[198:205], v[146:149], v234, v235 op_sel_hi:[0,0,0]
	v_mfma_scale_f32_16x16x128_f8f6f4 v[142:145], v[18:25], v[206:213], v[142:145], v234, v235 op_sel_hi:[0,0,0]
	v_mfma_scale_f32_16x16x128_f8f6f4 v[138:141], v[26:33], v[206:213], v[138:141], v234, v235 op_sel_hi:[0,0,0]
	v_mfma_scale_f32_16x16x128_f8f6f4 v[134:137], v[18:25], v[216:223], v[134:137], v234, v235 op_sel_hi:[0,0,0]
	v_mfma_scale_f32_16x16x128_f8f6f4 v[130:133], v[26:33], v[216:223], v[130:133], v234, v235 op_sel_hi:[0,0,0]
	v_mfma_scale_f32_16x16x128_f8f6f4 v[126:129], v[18:25], v[224:231], v[126:129], v234, v235 op_sel_hi:[0,0,0]
	v_mfma_scale_f32_16x16x128_f8f6f4 v[122:125], v[26:33], v[224:231], v[122:125], v234, v235 op_sel_hi:[0,0,0]
	v_mfma_scale_f32_16x16x128_f8f6f4 v[118:121], v[2:9], v[198:205], v[118:121], v234, v235 op_sel_hi:[0,0,0]
	v_mfma_scale_f32_16x16x128_f8f6f4 v[114:117], v[10:17], v[198:205], v[114:117], v234, v235 op_sel_hi:[0,0,0]
	v_mfma_scale_f32_16x16x128_f8f6f4 v[110:113], v[2:9], v[206:213], v[110:113], v234, v235 op_sel_hi:[0,0,0]
	v_mfma_scale_f32_16x16x128_f8f6f4 v[106:109], v[10:17], v[206:213], v[106:109], v234, v235 op_sel_hi:[0,0,0]
	v_mfma_scale_f32_16x16x128_f8f6f4 v[102:105], v[2:9], v[216:223], v[102:105], v234, v235 op_sel_hi:[0,0,0]
	v_mfma_scale_f32_16x16x128_f8f6f4 v[98:101], v[10:17], v[216:223], v[98:101], v234, v235 op_sel_hi:[0,0,0]
	v_mfma_scale_f32_16x16x128_f8f6f4 v[94:97], v[2:9], v[224:231], v[94:97], v234, v235 op_sel_hi:[0,0,0]
	v_mfma_scale_f32_16x16x128_f8f6f4 v[90:93], v[10:17], v[224:231], v[90:93], v234, v235 op_sel_hi:[0,0,0]
	s_setprio 0
	s_barrier
	s_mov_b64 s[54:55], 0x180
	s_mov_b32 m0, s64
	v_lshl_add_u64 v[170:171], v[170:171], 0, s[54:55]
	ds_read_b128 v[198:201], v192 offset:49152
	ds_read_b128 v[202:205], v192 offset:50176
	ds_read_b128 v[206:209], v192 offset:51200
	ds_read_b128 v[210:213], v192 offset:52224
	ds_read_b128 v[216:219], v192 offset:53248
	ds_read_b128 v[220:223], v192 offset:54272
	ds_read_b128 v[224:227], v192 offset:55296
	ds_read_b128 v[228:231], v192 offset:56320
	global_load_lds_dwordx4 v[170:171], off
	v_lshl_add_u64 v[170:171], v[172:173], 0, s[54:55]
	s_add_u32 s54, s4, 0x20180
	s_mov_b32 m0, s81
	s_addc_u32 s55, s5, 0
	global_load_lds_dwordx4 v[170:171], off
	v_lshl_add_u64 v[170:171], s[54:55], 0, v[162:163]
	s_mov_b32 m0, s49
	s_nop 0
	global_load_lds_dwordx4 v[170:171], off
	v_lshl_add_u64 v[170:171], s[54:55], 0, v[164:165]
	s_mov_b32 m0, s30
	s_nop 0
	global_load_lds_dwordx4 v[170:171], off
	s_mov_b32 m0, s6
	s_nop 0
	global_load_lds_dwordx4 v0, s[36:37]
	s_mov_b32 m0, s7
	s_nop 0
	global_load_lds_dwordx4 v197, s[36:37]
	s_waitcnt vmcnt(8)
	s_waitcnt lgkmcnt(0)
	s_barrier
	s_setprio 1
	s_waitcnt lgkmcnt(0)
	v_mfma_scale_f32_16x16x128_f8f6f4 v[86:89], v[18:25], v[198:205], v[86:89], v234, v235 op_sel_hi:[0,0,0]
	v_mfma_scale_f32_16x16x128_f8f6f4 v[82:85], v[26:33], v[198:205], v[82:85], v234, v235 op_sel_hi:[0,0,0]
	v_mfma_scale_f32_16x16x128_f8f6f4 v[78:81], v[18:25], v[206:213], v[78:81], v234, v235 op_sel_hi:[0,0,0]
	v_mfma_scale_f32_16x16x128_f8f6f4 v[74:77], v[26:33], v[206:213], v[74:77], v234, v235 op_sel_hi:[0,0,0]
	v_mfma_scale_f32_16x16x128_f8f6f4 v[70:73], v[18:25], v[216:223], v[70:73], v234, v235 op_sel_hi:[0,0,0]
	v_mfma_scale_f32_16x16x128_f8f6f4 v[66:69], v[26:33], v[216:223], v[66:69], v234, v235 op_sel_hi:[0,0,0]
	v_mfma_scale_f32_16x16x128_f8f6f4 v[62:65], v[18:25], v[224:231], v[62:65], v234, v235 op_sel_hi:[0,0,0]
	v_mfma_scale_f32_16x16x128_f8f6f4 v[58:61], v[26:33], v[224:231], v[58:61], v234, v235 op_sel_hi:[0,0,0]
	v_mfma_scale_f32_16x16x128_f8f6f4 v[54:57], v[2:9], v[198:205], v[54:57], v234, v235 op_sel_hi:[0,0,0]
	v_mfma_scale_f32_16x16x128_f8f6f4 v[50:53], v[10:17], v[198:205], v[50:53], v234, v235 op_sel_hi:[0,0,0]
	v_mfma_scale_f32_16x16x128_f8f6f4 v[46:49], v[2:9], v[206:213], v[46:49], v234, v235 op_sel_hi:[0,0,0]
	v_mfma_scale_f32_16x16x128_f8f6f4 v[42:45], v[10:17], v[206:213], v[42:45], v234, v235 op_sel_hi:[0,0,0]
	v_mfma_scale_f32_16x16x128_f8f6f4 v[38:41], v[2:9], v[216:223], v[38:41], v234, v235 op_sel_hi:[0,0,0]
	v_mfma_scale_f32_16x16x128_f8f6f4 v[34:37], v[10:17], v[216:223], v[34:37], v234, v235 op_sel_hi:[0,0,0]
	v_mfma_scale_f32_16x16x128_f8f6f4 v[154:157], v[2:9], v[224:231], v[154:157], v234, v235 op_sel_hi:[0,0,0]
	v_mfma_scale_f32_16x16x128_f8f6f4 v[158:161], v[10:17], v[224:231], v[158:161], v234, v235 op_sel_hi:[0,0,0]
	s_setprio 0
	s_barrier
	s_add_u32 s43, s4, 0x200
	s_addc_u32 s45, s5, 0
	s_mov_b32 s74, 0
	s_mov_b64 s[54:55], s[36:37]
	s_branch .LBB0_2003
.LBB0_2002:
	ds_read_b128 v[2:5], v183
	ds_read_b128 v[6:9], v182
	ds_read_b128 v[10:13], v181
	ds_read_b128 v[14:17], v180
	ds_read_b128 v[26:29], v179
	ds_read_b128 v[30:33], v178
	ds_read_b128 v[198:201], v177
	ds_read_b128 v[202:205], v176
	s_add_u32 s58, s54, 0x80
	s_addc_u32 s59, s55, 0
	s_and_b64 s[56:57], s[4:5], exec
	s_cselect_b32 s59, s9, s59
	s_cselect_b32 s58, s8, s58
	s_cselect_b32 s57, s47, s45
	s_cselect_b32 s56, s46, s43
	s_mov_b32 m0, s27
	v_lshl_add_u64 v[170:171], s[54:55], 0, v[166:167]
	ds_read_b128 v[18:21], v192
	ds_read_b128 v[22:25], v192 offset:1024
	ds_read_b128 v[206:209], v192 offset:2048
	ds_read_b128 v[210:213], v192 offset:3072
	ds_read_b128 v[216:219], v192 offset:4096
	ds_read_b128 v[220:223], v192 offset:5120
	ds_read_b128 v[224:227], v192 offset:6144
	ds_read_b128 v[228:231], v192 offset:7168
	global_load_lds_dwordx4 v[170:171], off
	v_lshl_add_u64 v[170:171], s[54:55], 0, v[168:169]
	s_mov_b32 m0, s41
	s_nop 0
	global_load_lds_dwordx4 v[170:171], off
	s_waitcnt vmcnt(8)
	s_waitcnt lgkmcnt(0)
	s_barrier
	s_setprio 1
	s_waitcnt lgkmcnt(0)
	v_mfma_scale_f32_16x16x128_f8f6f4 v[150:153], v[2:9], v[18:25], v[150:153], v234, v235 op_sel_hi:[0,0,0]
	v_mfma_scale_f32_16x16x128_f8f6f4 v[146:149], v[10:17], v[18:25], v[146:149], v234, v235 op_sel_hi:[0,0,0]
	v_mfma_scale_f32_16x16x128_f8f6f4 v[142:145], v[2:9], v[206:213], v[142:145], v234, v235 op_sel_hi:[0,0,0]
	v_mfma_scale_f32_16x16x128_f8f6f4 v[138:141], v[10:17], v[206:213], v[138:141], v234, v235 op_sel_hi:[0,0,0]
	v_mfma_scale_f32_16x16x128_f8f6f4 v[134:137], v[2:9], v[216:223], v[134:137], v234, v235 op_sel_hi:[0,0,0]
	v_mfma_scale_f32_16x16x128_f8f6f4 v[130:133], v[10:17], v[216:223], v[130:133], v234, v235 op_sel_hi:[0,0,0]
	v_mfma_scale_f32_16x16x128_f8f6f4 v[126:129], v[2:9], v[224:231], v[126:129], v234, v235 op_sel_hi:[0,0,0]
	v_mfma_scale_f32_16x16x128_f8f6f4 v[122:125], v[10:17], v[224:231], v[122:125], v234, v235 op_sel_hi:[0,0,0]
	v_mfma_scale_f32_16x16x128_f8f6f4 v[118:121], v[26:33], v[18:25], v[118:121], v234, v235 op_sel_hi:[0,0,0]
	v_mfma_scale_f32_16x16x128_f8f6f4 v[114:117], v[198:205], v[18:25], v[114:117], v234, v235 op_sel_hi:[0,0,0]
	v_mfma_scale_f32_16x16x128_f8f6f4 v[110:113], v[26:33], v[206:213], v[110:113], v234, v235 op_sel_hi:[0,0,0]
	v_mfma_scale_f32_16x16x128_f8f6f4 v[106:109], v[198:205], v[206:213], v[106:109], v234, v235 op_sel_hi:[0,0,0]
	v_mfma_scale_f32_16x16x128_f8f6f4 v[102:105], v[26:33], v[216:223], v[102:105], v234, v235 op_sel_hi:[0,0,0]
	v_mfma_scale_f32_16x16x128_f8f6f4 v[98:101], v[198:205], v[216:223], v[98:101], v234, v235 op_sel_hi:[0,0,0]
	v_mfma_scale_f32_16x16x128_f8f6f4 v[94:97], v[26:33], v[224:231], v[94:97], v234, v235 op_sel_hi:[0,0,0]
	v_mfma_scale_f32_16x16x128_f8f6f4 v[90:93], v[198:205], v[224:231], v[90:93], v234, v235 op_sel_hi:[0,0,0]
	s_setprio 0
	s_barrier
	s_mov_b32 m0, s68
	v_lshl_add_u64 v[18:19], s[56:57], 0, v[162:163]
	s_add_u32 vcc_lo, s56, 0x20000
	ds_read_b128 v[206:209], v192 offset:16384
	ds_read_b128 v[210:213], v192 offset:17408
	ds_read_b128 v[216:219], v192 offset:18432
	ds_read_b128 v[220:223], v192 offset:19456
	ds_read_b128 v[224:227], v192 offset:20480
	ds_read_b128 v[228:231], v192 offset:21504
	ds_read_b128 v[244:247], v192 offset:22528
	ds_read_b128 v[248:251], v192 offset:23552
	global_load_lds_dwordx4 v[18:19], off
	v_lshl_add_u64 v[20:21], s[56:57], 0, v[164:165]
	s_mov_b32 m0, s60
	s_addc_u32 vcc_hi, s57, 0
	global_load_lds_dwordx4 v[20:21], off
	v_lshl_add_u64 v[22:23], vcc, 0, v[162:163]
	s_mov_b32 m0, s61
	s_nop 0
	global_load_lds_dwordx4 v[22:23], off
	v_lshl_add_u64 v[22:23], vcc, 0, v[164:165]
	s_mov_b32 m0, s62
	s_nop 0
	global_load_lds_dwordx4 v[22:23], off
	v_cndmask_b32_e64 v22, v195, v193, s[4:5]
	v_lshlrev_b32_e32 v0, 10, v22
	v_and_or_b32 v0, v0, s82, v174
	v_bfe_u32 v22, v22, 16, 16
	s_mov_b32 m0, s65
	v_lshl_add_u32 v22, v22, 10, v175
	global_load_lds_dwordx4 v0, s[58:59]
	s_mov_b32 m0, s63
	v_mov_b32_e32 v23, v1
	global_load_lds_dwordx4 v22, s[58:59]
	s_waitcnt vmcnt(8)
	s_waitcnt lgkmcnt(0)
	v_lshl_add_u64 v[24:25], s[58:59], 0, v[0:1]
	v_lshl_add_u64 v[22:23], s[58:59], 0, v[22:23]
	s_barrier
	s_setprio 1
	s_waitcnt lgkmcnt(0)
	v_mfma_scale_f32_16x16x128_f8f6f4 v[86:89], v[2:9], v[206:213], v[86:89], v234, v235 op_sel_hi:[0,0,0]
	v_mfma_scale_f32_16x16x128_f8f6f4 v[82:85], v[10:17], v[206:213], v[82:85], v234, v235 op_sel_hi:[0,0,0]
	v_mfma_scale_f32_16x16x128_f8f6f4 v[78:81], v[2:9], v[216:223], v[78:81], v234, v235 op_sel_hi:[0,0,0]
	v_mfma_scale_f32_16x16x128_f8f6f4 v[74:77], v[10:17], v[216:223], v[74:77], v234, v235 op_sel_hi:[0,0,0]
	v_mfma_scale_f32_16x16x128_f8f6f4 v[70:73], v[2:9], v[224:231], v[70:73], v234, v235 op_sel_hi:[0,0,0]
	v_mfma_scale_f32_16x16x128_f8f6f4 v[66:69], v[10:17], v[224:231], v[66:69], v234, v235 op_sel_hi:[0,0,0]
	v_mfma_scale_f32_16x16x128_f8f6f4 v[62:65], v[2:9], v[244:251], v[62:65], v234, v235 op_sel_hi:[0,0,0]
	v_mfma_scale_f32_16x16x128_f8f6f4 v[58:61], v[10:17], v[244:251], v[58:61], v234, v235 op_sel_hi:[0,0,0]
	v_mfma_scale_f32_16x16x128_f8f6f4 v[54:57], v[26:33], v[206:213], v[54:57], v234, v235 op_sel_hi:[0,0,0]
	v_mfma_scale_f32_16x16x128_f8f6f4 v[50:53], v[198:205], v[206:213], v[50:53], v234, v235 op_sel_hi:[0,0,0]
	v_mfma_scale_f32_16x16x128_f8f6f4 v[46:49], v[26:33], v[216:223], v[46:49], v234, v235 op_sel_hi:[0,0,0]
	v_mfma_scale_f32_16x16x128_f8f6f4 v[42:45], v[198:205], v[216:223], v[42:45], v234, v235 op_sel_hi:[0,0,0]
	v_mfma_scale_f32_16x16x128_f8f6f4 v[38:41], v[26:33], v[224:231], v[38:41], v234, v235 op_sel_hi:[0,0,0]
	v_mfma_scale_f32_16x16x128_f8f6f4 v[34:37], v[198:205], v[224:231], v[34:37], v234, v235 op_sel_hi:[0,0,0]
	v_mfma_scale_f32_16x16x128_f8f6f4 v[154:157], v[26:33], v[244:251], v[154:157], v234, v235 op_sel_hi:[0,0,0]
	v_mfma_scale_f32_16x16x128_f8f6f4 v[158:161], v[198:205], v[244:251], v[158:161], v234, v235 op_sel_hi:[0,0,0]
	s_setprio 0
	s_barrier
	ds_read_b128 v[10:13], v184
	ds_read_b128 v[14:17], v185
	ds_read_b128 v[26:29], v186
	ds_read_b128 v[30:33], v187
	ds_read_b128 v[2:5], v188
	ds_read_b128 v[6:9], v189
	ds_read_b128 v[198:201], v190
	ds_read_b128 v[202:205], v191
	v_cndmask_b32_e64 v0, v196, v194, s[4:5]
	v_lshlrev_b32_e32 v170, 10, v0
	s_mov_b32 m0, s10
	v_and_or_b32 v170, v170, s82, v174
	v_bfe_u32 v0, v0, 16, 16
	ds_read_b128 v[206:209], v192 offset:32768
	ds_read_b128 v[210:213], v192 offset:33792
	ds_read_b128 v[216:219], v192 offset:34816
	ds_read_b128 v[220:223], v192 offset:35840
	ds_read_b128 v[224:227], v192 offset:36864
	ds_read_b128 v[228:231], v192 offset:37888
	ds_read_b128 v[244:247], v192 offset:38912
	ds_read_b128 v[248:251], v192 offset:39936
	v_lshl_add_u32 v0, v0, 10, v175
	global_load_lds_dwordx4 v170, s[58:59]
	s_mov_b32 m0, s11
	s_nop 0
	global_load_lds_dwordx4 v0, s[58:59]
	s_waitcnt vmcnt(8)
	s_waitcnt lgkmcnt(0)
	s_barrier
	s_setprio 1
	s_waitcnt lgkmcnt(0)
	v_mfma_scale_f32_16x16x128_f8f6f4 v[150:153], v[10:17], v[206:213], v[150:153], v234, v235 op_sel_hi:[0,0,0]
	v_mfma_scale_f32_16x16x128_f8f6f4 v[146:149], v[26:33], v[206:213], v[146:149], v234, v235 op_sel_hi:[0,0,0]
	v_mfma_scale_f32_16x16x128_f8f6f4 v[142:145], v[10:17], v[216:223], v[142:145], v234, v235 op_sel_hi:[0,0,0]
	v_mfma_scale_f32_16x16x128_f8f6f4 v[138:141], v[26:33], v[216:223], v[138:141], v234, v235 op_sel_hi:[0,0,0]
	v_mfma_scale_f32_16x16x128_f8f6f4 v[134:137], v[10:17], v[224:231], v[134:137], v234, v235 op_sel_hi:[0,0,0]
	v_mfma_scale_f32_16x16x128_f8f6f4 v[130:133], v[26:33], v[224:231], v[130:133], v234, v235 op_sel_hi:[0,0,0]
	v_mfma_scale_f32_16x16x128_f8f6f4 v[126:129], v[10:17], v[244:251], v[126:129], v234, v235 op_sel_hi:[0,0,0]
	v_mfma_scale_f32_16x16x128_f8f6f4 v[122:125], v[26:33], v[244:251], v[122:125], v234, v235 op_sel_hi:[0,0,0]
	v_mfma_scale_f32_16x16x128_f8f6f4 v[118:121], v[2:9], v[206:213], v[118:121], v234, v235 op_sel_hi:[0,0,0]
	v_mfma_scale_f32_16x16x128_f8f6f4 v[114:117], v[198:205], v[206:213], v[114:117], v234, v235 op_sel_hi:[0,0,0]
	v_mfma_scale_f32_16x16x128_f8f6f4 v[110:113], v[2:9], v[216:223], v[110:113], v234, v235 op_sel_hi:[0,0,0]
	v_mfma_scale_f32_16x16x128_f8f6f4 v[106:109], v[198:205], v[216:223], v[106:109], v234, v235 op_sel_hi:[0,0,0]
	v_mfma_scale_f32_16x16x128_f8f6f4 v[102:105], v[2:9], v[224:231], v[102:105], v234, v235 op_sel_hi:[0,0,0]
	v_mfma_scale_f32_16x16x128_f8f6f4 v[98:101], v[198:205], v[224:231], v[98:101], v234, v235 op_sel_hi:[0,0,0]
	v_mfma_scale_f32_16x16x128_f8f6f4 v[94:97], v[2:9], v[244:251], v[94:97], v234, v235 op_sel_hi:[0,0,0]
	v_mfma_scale_f32_16x16x128_f8f6f4 v[90:93], v[198:205], v[244:251], v[90:93], v234, v235 op_sel_hi:[0,0,0]
	s_setprio 0
	s_barrier
	s_mov_b32 m0, s64
	v_lshl_add_u64 v[18:19], v[18:19], 0, s[66:67]
	s_add_u32 s4, s56, 0x20080
	ds_read_b128 v[206:209], v192 offset:49152
	ds_read_b128 v[210:213], v192 offset:50176
	ds_read_b128 v[216:219], v192 offset:51200
	ds_read_b128 v[220:223], v192 offset:52224
	ds_read_b128 v[224:227], v192 offset:53248
	ds_read_b128 v[228:231], v192 offset:54272
	ds_read_b128 v[244:247], v192 offset:55296
	ds_read_b128 v[248:251], v192 offset:56320
	global_load_lds_dwordx4 v[18:19], off
	v_lshl_add_u64 v[18:19], v[20:21], 0, s[66:67]
	s_mov_b32 m0, s81
	s_addc_u32 s5, s57, 0
	global_load_lds_dwordx4 v[18:19], off
	v_lshl_add_u64 v[18:19], s[4:5], 0, v[162:163]
	s_mov_b32 m0, s49
	s_nop 0
	global_load_lds_dwordx4 v[18:19], off
	v_lshl_add_u64 v[18:19], s[4:5], 0, v[164:165]
	s_mov_b32 m0, s30
	s_nop 0
	global_load_lds_dwordx4 v[18:19], off
	v_lshl_add_u64 v[18:19], v[24:25], 0, s[66:67]
	s_mov_b32 m0, s6
	s_nop 0
	global_load_lds_dwordx4 v[18:19], off
	v_lshl_add_u64 v[18:19], v[22:23], 0, s[66:67]
	s_mov_b32 m0, s7
	s_nop 0
	global_load_lds_dwordx4 v[18:19], off
	s_waitcnt vmcnt(8)
	s_waitcnt lgkmcnt(0)
	s_barrier
	s_setprio 1
	s_waitcnt lgkmcnt(0)
	v_mfma_scale_f32_16x16x128_f8f6f4 v[86:89], v[10:17], v[206:213], v[86:89], v234, v235 op_sel_hi:[0,0,0]
	v_mfma_scale_f32_16x16x128_f8f6f4 v[82:85], v[26:33], v[206:213], v[82:85], v234, v235 op_sel_hi:[0,0,0]
	v_mfma_scale_f32_16x16x128_f8f6f4 v[78:81], v[10:17], v[216:223], v[78:81], v234, v235 op_sel_hi:[0,0,0]
	v_mfma_scale_f32_16x16x128_f8f6f4 v[74:77], v[26:33], v[216:223], v[74:77], v234, v235 op_sel_hi:[0,0,0]
	v_mfma_scale_f32_16x16x128_f8f6f4 v[70:73], v[10:17], v[224:231], v[70:73], v234, v235 op_sel_hi:[0,0,0]
	v_mfma_scale_f32_16x16x128_f8f6f4 v[66:69], v[26:33], v[224:231], v[66:69], v234, v235 op_sel_hi:[0,0,0]
	v_mfma_scale_f32_16x16x128_f8f6f4 v[62:65], v[10:17], v[244:251], v[62:65], v234, v235 op_sel_hi:[0,0,0]
	v_mfma_scale_f32_16x16x128_f8f6f4 v[58:61], v[26:33], v[244:251], v[58:61], v234, v235 op_sel_hi:[0,0,0]
	v_mfma_scale_f32_16x16x128_f8f6f4 v[54:57], v[2:9], v[206:213], v[54:57], v234, v235 op_sel_hi:[0,0,0]
	v_mfma_scale_f32_16x16x128_f8f6f4 v[50:53], v[198:205], v[206:213], v[50:53], v234, v235 op_sel_hi:[0,0,0]
	v_mfma_scale_f32_16x16x128_f8f6f4 v[46:49], v[2:9], v[216:223], v[46:49], v234, v235 op_sel_hi:[0,0,0]
	v_mfma_scale_f32_16x16x128_f8f6f4 v[42:45], v[198:205], v[216:223], v[42:45], v234, v235 op_sel_hi:[0,0,0]
	v_mfma_scale_f32_16x16x128_f8f6f4 v[38:41], v[2:9], v[224:231], v[38:41], v234, v235 op_sel_hi:[0,0,0]
	v_mfma_scale_f32_16x16x128_f8f6f4 v[34:37], v[198:205], v[224:231], v[34:37], v234, v235 op_sel_hi:[0,0,0]
	v_mfma_scale_f32_16x16x128_f8f6f4 v[154:157], v[2:9], v[244:251], v[154:157], v234, v235 op_sel_hi:[0,0,0]
	v_mfma_scale_f32_16x16x128_f8f6f4 v[158:161], v[198:205], v[244:251], v[158:161], v234, v235 op_sel_hi:[0,0,0]
	s_setprio 0
	s_barrier
	s_add_i32 s74, s74, 2
	s_add_u32 s54, s54, 0x100
	s_addc_u32 s55, s55, 0
	s_add_u32 s43, s43, 0x100
	s_addc_u32 s45, s45, 0
	s_cmp_gt_u32 s74, 5
	s_cbranch_scc1 .LBB0_2005

.Lrw_done_g2_0:
	s_waitcnt lgkmcnt(0)
	s_barrier
	s_setprio 1
	s_waitcnt lgkmcnt(0)
	v_mfma_scale_f32_16x16x128_f8f6f4 v[158:161], v[18:25], v[172:179], 0, v234, v238 op_sel_hi:[0,0,0]
	v_mfma_scale_f32_16x16x128_f8f6f4 v[154:157], v[26:33], v[172:179], 0, v234, v238 op_sel_hi:[0,0,0]
	v_mfma_scale_f32_16x16x128_f8f6f4 v[150:153], v[18:25], v[198:205], 0, v234, v238 op_sel_hi:[0,0,0]
	v_mfma_scale_f32_16x16x128_f8f6f4 v[146:149], v[26:33], v[198:205], 0, v234, v238 op_sel_hi:[0,0,0]
	v_mfma_scale_f32_16x16x128_f8f6f4 v[142:145], v[18:25], v[206:213], 0, v234, v238 op_sel_hi:[0,0,0]
	v_mfma_scale_f32_16x16x128_f8f6f4 v[138:141], v[26:33], v[206:213], 0, v234, v238 op_sel_hi:[0,0,0]
	v_mfma_scale_f32_16x16x128_f8f6f4 v[134:137], v[18:25], v[216:223], 0, v234, v238 op_sel_hi:[0,0,0]
	v_mfma_scale_f32_16x16x128_f8f6f4 v[130:133], v[26:33], v[216:223], 0, v234, v238 op_sel_hi:[0,0,0]
	v_mfma_scale_f32_16x16x128_f8f6f4 v[126:129], v[2:9], v[172:179], 0, v234, v238 op_sel_hi:[0,0,0]
	v_mfma_scale_f32_16x16x128_f8f6f4 v[122:125], v[10:17], v[172:179], 0, v234, v238 op_sel_hi:[0,0,0]
	v_mfma_scale_f32_16x16x128_f8f6f4 v[118:121], v[2:9], v[198:205], 0, v234, v238 op_sel_hi:[0,0,0]
	v_mfma_scale_f32_16x16x128_f8f6f4 v[114:117], v[10:17], v[198:205], 0, v234, v238 op_sel_hi:[0,0,0]
	v_mfma_scale_f32_16x16x128_f8f6f4 v[110:113], v[2:9], v[206:213], 0, v234, v238 op_sel_hi:[0,0,0]
	v_mfma_scale_f32_16x16x128_f8f6f4 v[106:109], v[10:17], v[206:213], 0, v234, v238 op_sel_hi:[0,0,0]
	v_mfma_scale_f32_16x16x128_f8f6f4 v[102:105], v[2:9], v[216:223], 0, v234, v238 op_sel_hi:[0,0,0]
	v_mfma_scale_f32_16x16x128_f8f6f4 v[98:101], v[10:17], v[216:223], 0, v234, v238 op_sel_hi:[0,0,0]
	s_setprio 0
	s_barrier
	v_lshl_add_u64 v[172:173], s[44:45], 0, v[0:1]
	s_mov_b64 s[48:49], 0x100
	s_mov_b32 m0, s41
	v_lshl_add_u64 v[174:175], v[172:173], 0, s[48:49]
	ds_read_b128 v[198:201], v196 offset:16384
	ds_read_b128 v[202:205], v196 offset:17408
	ds_read_b128 v[206:209], v196 offset:18432
	ds_read_b128 v[210:213], v196 offset:19456
	ds_read_b128 v[216:219], v196 offset:20480
	ds_read_b128 v[220:223], v196 offset:21504
	ds_read_b128 v[224:227], v196 offset:22528
	ds_read_b128 v[228:231], v196 offset:23552
	global_load_lds_dwordx4 v[174:175], off
	v_lshl_add_u64 v[174:175], s[44:45], 0, v[166:167]
	s_add_u32 s46, s44, 0x20100
	v_lshl_add_u64 v[176:177], v[174:175], 0, s[48:49]
	s_mov_b32 m0, s57
	s_addc_u32 s47, s45, 0
	global_load_lds_dwordx4 v[176:177], off
	v_lshl_add_u64 v[176:177], s[46:47], 0, v[0:1]
	s_mov_b32 m0, s58
	s_nop 0
	global_load_lds_dwordx4 v[176:177], off
	v_lshl_add_u64 v[176:177], s[46:47], 0, v[166:167]
	s_mov_b32 m0, s59
	s_nop 0
	global_load_lds_dwordx4 v[176:177], off
	v_lshl_add_u64 v[176:177], s[42:43], 0, v[162:163]
	v_lshl_add_u64 v[178:179], v[176:177], 0, s[48:49]
	s_mov_b32 m0, s37
	s_nop 0
	global_load_lds_dwordx4 v[178:179], off
	v_lshl_add_u64 v[178:179], s[42:43], 0, v[164:165]
	v_lshl_add_u64 v[232:233], v[178:179], 0, s[48:49]
	s_mov_b32 m0, s60
	s_nop 0
	global_load_lds_dwordx4 v[232:233], off
	s_cmp_eq_u32 s26, 0
	s_cbranch_scc1 .Lrw_first_g2_1
	s_waitcnt vmcnt(24)
	s_branch .Lrw_done_g2_1

.Lrw_done_g2_1:
	s_waitcnt lgkmcnt(0)
	s_barrier
	s_setprio 1
	s_waitcnt lgkmcnt(0)
	v_mfma_scale_f32_16x16x128_f8f6f4 v[94:97], v[18:25], v[198:205], 0, v234, v238 op_sel_hi:[0,0,0]
	v_mfma_scale_f32_16x16x128_f8f6f4 v[90:93], v[26:33], v[198:205], 0, v234, v238 op_sel_hi:[0,0,0]
	v_mfma_scale_f32_16x16x128_f8f6f4 v[86:89], v[18:25], v[206:213], 0, v234, v238 op_sel_hi:[0,0,0]
	v_mfma_scale_f32_16x16x128_f8f6f4 v[82:85], v[26:33], v[206:213], 0, v234, v238 op_sel_hi:[0,0,0]
	v_mfma_scale_f32_16x16x128_f8f6f4 v[78:81], v[18:25], v[216:223], 0, v234, v238 op_sel_hi:[0,0,0]
	v_mfma_scale_f32_16x16x128_f8f6f4 v[74:77], v[26:33], v[216:223], 0, v234, v238 op_sel_hi:[0,0,0]
	v_mfma_scale_f32_16x16x128_f8f6f4 v[70:73], v[18:25], v[224:231], 0, v234, v238 op_sel_hi:[0,0,0]
	v_mfma_scale_f32_16x16x128_f8f6f4 v[66:69], v[26:33], v[224:231], 0, v234, v238 op_sel_hi:[0,0,0]
	v_mfma_scale_f32_16x16x128_f8f6f4 v[62:65], v[2:9], v[198:205], 0, v234, v238 op_sel_hi:[0,0,0]
	v_mfma_scale_f32_16x16x128_f8f6f4 v[58:61], v[10:17], v[198:205], 0, v234, v238 op_sel_hi:[0,0,0]
	v_mfma_scale_f32_16x16x128_f8f6f4 v[54:57], v[2:9], v[206:213], 0, v234, v238 op_sel_hi:[0,0,0]
	v_mfma_scale_f32_16x16x128_f8f6f4 v[50:53], v[10:17], v[206:213], 0, v234, v238 op_sel_hi:[0,0,0]
	v_mfma_scale_f32_16x16x128_f8f6f4 v[46:49], v[2:9], v[216:223], 0, v234, v238 op_sel_hi:[0,0,0]
	v_mfma_scale_f32_16x16x128_f8f6f4 v[42:45], v[10:17], v[216:223], 0, v234, v238 op_sel_hi:[0,0,0]
	v_mfma_scale_f32_16x16x128_f8f6f4 v[38:41], v[2:9], v[224:231], 0, v234, v238 op_sel_hi:[0,0,0]
	v_mfma_scale_f32_16x16x128_f8f6f4 v[34:37], v[10:17], v[224:231], 0, v234, v238 op_sel_hi:[0,0,0]
	s_setprio 0
	s_barrier
	ds_read_b128 v[18:21], v188
	ds_read_b128 v[22:25], v189
	ds_read_b128 v[26:29], v190
	ds_read_b128 v[30:33], v191
	ds_read_b128 v[2:5], v192
	ds_read_b128 v[6:9], v193
	ds_read_b128 v[10:13], v194
	ds_read_b128 v[14:17], v195
	s_add_u32 s46, s42, 0x20100
	s_addc_u32 s47, s43, 0
	s_mov_b32 m0, s61
	v_lshl_add_u64 v[232:233], s[46:47], 0, v[162:163]
	ds_read_b128 v[198:201], v196 offset:32768
	ds_read_b128 v[202:205], v196 offset:33792
	ds_read_b128 v[206:209], v196 offset:34816
	ds_read_b128 v[210:213], v196 offset:35840
	ds_read_b128 v[216:219], v196 offset:36864
	ds_read_b128 v[220:223], v196 offset:37888
	ds_read_b128 v[224:227], v196 offset:38912
	ds_read_b128 v[228:231], v196 offset:39936
	global_load_lds_dwordx4 v[232:233], off
	v_lshl_add_u64 v[232:233], s[46:47], 0, v[164:165]
	s_mov_b32 m0, s62
	s_nop 0
	global_load_lds_dwordx4 v[232:233], off
	s_waitcnt vmcnt(8)
	s_waitcnt lgkmcnt(0)
	s_barrier
	s_setprio 1
	s_waitcnt lgkmcnt(0)
	v_mfma_scale_f32_16x16x128_f8f6f4 v[158:161], v[18:25], v[198:205], v[158:161], v234, v238 op_sel_hi:[0,0,0]
	v_mfma_scale_f32_16x16x128_f8f6f4 v[154:157], v[26:33], v[198:205], v[154:157], v234, v238 op_sel_hi:[0,0,0]
	v_mfma_scale_f32_16x16x128_f8f6f4 v[150:153], v[18:25], v[206:213], v[150:153], v234, v238 op_sel_hi:[0,0,0]
	v_mfma_scale_f32_16x16x128_f8f6f4 v[146:149], v[26:33], v[206:213], v[146:149], v234, v238 op_sel_hi:[0,0,0]
	v_mfma_scale_f32_16x16x128_f8f6f4 v[142:145], v[18:25], v[216:223], v[142:145], v234, v238 op_sel_hi:[0,0,0]
	v_mfma_scale_f32_16x16x128_f8f6f4 v[138:141], v[26:33], v[216:223], v[138:141], v234, v238 op_sel_hi:[0,0,0]
	v_mfma_scale_f32_16x16x128_f8f6f4 v[134:137], v[18:25], v[224:231], v[134:137], v234, v238 op_sel_hi:[0,0,0]
	v_mfma_scale_f32_16x16x128_f8f6f4 v[130:133], v[26:33], v[224:231], v[130:133], v234, v238 op_sel_hi:[0,0,0]
	v_mfma_scale_f32_16x16x128_f8f6f4 v[126:129], v[2:9], v[198:205], v[126:129], v234, v238 op_sel_hi:[0,0,0]
	v_mfma_scale_f32_16x16x128_f8f6f4 v[122:125], v[10:17], v[198:205], v[122:125], v234, v238 op_sel_hi:[0,0,0]
	v_mfma_scale_f32_16x16x128_f8f6f4 v[118:121], v[2:9], v[206:213], v[118:121], v234, v238 op_sel_hi:[0,0,0]
	v_mfma_scale_f32_16x16x128_f8f6f4 v[114:117], v[10:17], v[206:213], v[114:117], v234, v238 op_sel_hi:[0,0,0]
	v_mfma_scale_f32_16x16x128_f8f6f4 v[110:113], v[2:9], v[216:223], v[110:113], v234, v238 op_sel_hi:[0,0,0]
	v_mfma_scale_f32_16x16x128_f8f6f4 v[106:109], v[10:17], v[216:223], v[106:109], v234, v238 op_sel_hi:[0,0,0]
	v_mfma_scale_f32_16x16x128_f8f6f4 v[102:105], v[2:9], v[224:231], v[102:105], v234, v238 op_sel_hi:[0,0,0]
	v_mfma_scale_f32_16x16x128_f8f6f4 v[98:101], v[10:17], v[224:231], v[98:101], v234, v238 op_sel_hi:[0,0,0]
	s_setprio 0
	s_barrier
	s_mov_b64 s[48:49], 0x180
	s_mov_b32 m0, s65
	v_lshl_add_u64 v[172:173], v[172:173], 0, s[48:49]
	s_add_u32 s46, s44, 0x20180
	ds_read_b128 v[198:201], v196 offset:49152
	ds_read_b128 v[202:205], v196 offset:50176
	ds_read_b128 v[206:209], v196 offset:51200
	ds_read_b128 v[210:213], v196 offset:52224
	ds_read_b128 v[216:219], v196 offset:53248
	ds_read_b128 v[220:223], v196 offset:54272
	ds_read_b128 v[224:227], v196 offset:55296
	ds_read_b128 v[228:231], v196 offset:56320
	global_load_lds_dwordx4 v[172:173], off
	v_lshl_add_u64 v[172:173], v[174:175], 0, s[48:49]
	s_mov_b32 m0, s68
	s_addc_u32 s47, s45, 0
	global_load_lds_dwordx4 v[172:173], off
	v_lshl_add_u64 v[172:173], s[46:47], 0, v[0:1]
	s_mov_b32 m0, s51
	s_nop 0
	global_load_lds_dwordx4 v[172:173], off
	v_lshl_add_u64 v[172:173], s[46:47], 0, v[166:167]
	s_mov_b32 m0, s4
	s_nop 0
	global_load_lds_dwordx4 v[172:173], off
	v_lshl_add_u64 v[172:173], v[176:177], 0, s[48:49]
	s_mov_b32 m0, s81
	s_nop 0
	global_load_lds_dwordx4 v[172:173], off
	v_lshl_add_u64 v[172:173], v[178:179], 0, s[48:49]
	s_mov_b32 m0, s50
	s_nop 0
	global_load_lds_dwordx4 v[172:173], off
	s_waitcnt vmcnt(8)
	s_waitcnt lgkmcnt(0)
	s_barrier
	s_setprio 1
	s_waitcnt lgkmcnt(0)
	v_mfma_scale_f32_16x16x128_f8f6f4 v[94:97], v[18:25], v[198:205], v[94:97], v234, v238 op_sel_hi:[0,0,0]
	v_mfma_scale_f32_16x16x128_f8f6f4 v[90:93], v[26:33], v[198:205], v[90:93], v234, v238 op_sel_hi:[0,0,0]
	v_mfma_scale_f32_16x16x128_f8f6f4 v[86:89], v[18:25], v[206:213], v[86:89], v234, v238 op_sel_hi:[0,0,0]
	v_mfma_scale_f32_16x16x128_f8f6f4 v[82:85], v[26:33], v[206:213], v[82:85], v234, v238 op_sel_hi:[0,0,0]
	v_mfma_scale_f32_16x16x128_f8f6f4 v[78:81], v[18:25], v[216:223], v[78:81], v234, v238 op_sel_hi:[0,0,0]
	v_mfma_scale_f32_16x16x128_f8f6f4 v[74:77], v[26:33], v[216:223], v[74:77], v234, v238 op_sel_hi:[0,0,0]
	v_mfma_scale_f32_16x16x128_f8f6f4 v[70:73], v[18:25], v[224:231], v[70:73], v234, v238 op_sel_hi:[0,0,0]
	v_mfma_scale_f32_16x16x128_f8f6f4 v[66:69], v[26:33], v[224:231], v[66:69], v234, v238 op_sel_hi:[0,0,0]
	v_mfma_scale_f32_16x16x128_f8f6f4 v[62:65], v[2:9], v[198:205], v[62:65], v234, v238 op_sel_hi:[0,0,0]
	v_mfma_scale_f32_16x16x128_f8f6f4 v[58:61], v[10:17], v[198:205], v[58:61], v234, v238 op_sel_hi:[0,0,0]
	v_mfma_scale_f32_16x16x128_f8f6f4 v[54:57], v[2:9], v[206:213], v[54:57], v234, v238 op_sel_hi:[0,0,0]
	v_mfma_scale_f32_16x16x128_f8f6f4 v[50:53], v[10:17], v[206:213], v[50:53], v234, v238 op_sel_hi:[0,0,0]
	v_mfma_scale_f32_16x16x128_f8f6f4 v[46:49], v[2:9], v[216:223], v[46:49], v234, v238 op_sel_hi:[0,0,0]
	v_mfma_scale_f32_16x16x128_f8f6f4 v[42:45], v[10:17], v[216:223], v[42:45], v234, v238 op_sel_hi:[0,0,0]
	v_mfma_scale_f32_16x16x128_f8f6f4 v[38:41], v[2:9], v[224:231], v[38:41], v234, v238 op_sel_hi:[0,0,0]
	v_mfma_scale_f32_16x16x128_f8f6f4 v[34:37], v[10:17], v[224:231], v[34:37], v234, v238 op_sel_hi:[0,0,0]
	s_setprio 0
	s_barrier
	s_add_u32 s42, s42, 0x20180
	s_addc_u32 s43, s43, 0
	s_add_u32 s48, s44, 0x200
	s_addc_u32 s49, s45, 0
	s_mov_b32 s74, 0
.LBB0_2089:
	ds_read_b128 v[2:5], v180
	ds_read_b128 v[6:9], v181
	ds_read_b128 v[10:13], v182
	ds_read_b128 v[14:17], v183
	ds_read_b128 v[26:29], v184
	ds_read_b128 v[30:33], v185
	ds_read_b128 v[172:175], v186
	ds_read_b128 v[176:179], v187
	s_add_u32 s44, s42, 0xfffe0080
	s_addc_u32 s45, s43, -1
	s_cmp_eq_u32 s74, 4
	s_cselect_b32 s47, s13, s45
	s_cselect_b32 s46, s27, s44
	s_cselect_b32 s45, s35, s49
	s_cselect_b32 s44, s34, s48
	s_mov_b32 m0, s29
	v_lshl_add_u64 v[224:225], s[42:43], 0, v[168:169]
	ds_read_b128 v[18:21], v196
	ds_read_b128 v[22:25], v196 offset:1024
	ds_read_b128 v[198:201], v196 offset:2048
	ds_read_b128 v[202:205], v196 offset:3072
	ds_read_b128 v[206:209], v196 offset:4096
	ds_read_b128 v[210:213], v196 offset:5120
	ds_read_b128 v[216:219], v196 offset:6144
	ds_read_b128 v[220:223], v196 offset:7168
	global_load_lds_dwordx4 v[224:225], off
	v_lshl_add_u64 v[224:225], s[42:43], 0, v[170:171]
	s_mov_b32 m0, s31
	s_nop 0
	global_load_lds_dwordx4 v[224:225], off
	s_waitcnt vmcnt(8)
	s_waitcnt lgkmcnt(0)
	s_barrier
	s_setprio 1
	s_waitcnt lgkmcnt(0)
	v_mfma_scale_f32_16x16x128_f8f6f4 v[158:161], v[2:9], v[18:25], v[158:161], v234, v238 op_sel_hi:[0,0,0]
	v_mfma_scale_f32_16x16x128_f8f6f4 v[154:157], v[10:17], v[18:25], v[154:157], v234, v238 op_sel_hi:[0,0,0]
	v_mfma_scale_f32_16x16x128_f8f6f4 v[150:153], v[2:9], v[198:205], v[150:153], v234, v238 op_sel_hi:[0,0,0]
	v_mfma_scale_f32_16x16x128_f8f6f4 v[146:149], v[10:17], v[198:205], v[146:149], v234, v238 op_sel_hi:[0,0,0]
	v_mfma_scale_f32_16x16x128_f8f6f4 v[142:145], v[2:9], v[206:213], v[142:145], v234, v238 op_sel_hi:[0,0,0]
	v_mfma_scale_f32_16x16x128_f8f6f4 v[138:141], v[10:17], v[206:213], v[138:141], v234, v238 op_sel_hi:[0,0,0]
	v_mfma_scale_f32_16x16x128_f8f6f4 v[134:137], v[2:9], v[216:223], v[134:137], v234, v238 op_sel_hi:[0,0,0]
	v_mfma_scale_f32_16x16x128_f8f6f4 v[130:133], v[10:17], v[216:223], v[130:133], v234, v238 op_sel_hi:[0,0,0]
	v_mfma_scale_f32_16x16x128_f8f6f4 v[126:129], v[26:33], v[18:25], v[126:129], v234, v238 op_sel_hi:[0,0,0]
	v_mfma_scale_f32_16x16x128_f8f6f4 v[122:125], v[172:179], v[18:25], v[122:125], v234, v238 op_sel_hi:[0,0,0]
	v_mfma_scale_f32_16x16x128_f8f6f4 v[118:121], v[26:33], v[198:205], v[118:121], v234, v238 op_sel_hi:[0,0,0]
	v_mfma_scale_f32_16x16x128_f8f6f4 v[114:117], v[172:179], v[198:205], v[114:117], v234, v238 op_sel_hi:[0,0,0]
	v_mfma_scale_f32_16x16x128_f8f6f4 v[110:113], v[26:33], v[206:213], v[110:113], v234, v238 op_sel_hi:[0,0,0]
	v_mfma_scale_f32_16x16x128_f8f6f4 v[106:109], v[172:179], v[206:213], v[106:109], v234, v238 op_sel_hi:[0,0,0]
	v_mfma_scale_f32_16x16x128_f8f6f4 v[102:105], v[26:33], v[216:223], v[102:105], v234, v238 op_sel_hi:[0,0,0]
	v_mfma_scale_f32_16x16x128_f8f6f4 v[98:101], v[172:179], v[216:223], v[98:101], v234, v238 op_sel_hi:[0,0,0]
	s_setprio 0
	s_barrier
	s_mov_b32 m0, s41
	v_lshl_add_u64 v[18:19], s[44:45], 0, v[0:1]
	s_add_u32 vcc_lo, s44, 0x20000
	ds_read_b128 v[198:201], v196 offset:16384
	ds_read_b128 v[202:205], v196 offset:17408
	ds_read_b128 v[206:209], v196 offset:18432
	ds_read_b128 v[210:213], v196 offset:19456
	ds_read_b128 v[216:219], v196 offset:20480
	ds_read_b128 v[220:223], v196 offset:21504
	ds_read_b128 v[224:227], v196 offset:22528
	ds_read_b128 v[228:231], v196 offset:23552
	global_load_lds_dwordx4 v[18:19], off
	v_lshl_add_u64 v[20:21], s[44:45], 0, v[166:167]
	s_mov_b32 m0, s57
	s_addc_u32 vcc_hi, s45, 0
	global_load_lds_dwordx4 v[20:21], off
	v_lshl_add_u64 v[22:23], vcc, 0, v[0:1]
	s_mov_b32 m0, s58
	v_lshl_add_u64 v[24:25], s[46:47], 0, v[164:165]
	global_load_lds_dwordx4 v[22:23], off
	v_lshl_add_u64 v[22:23], vcc, 0, v[166:167]
	s_mov_b32 m0, s59
	s_nop 0
	global_load_lds_dwordx4 v[22:23], off
	v_lshl_add_u64 v[22:23], s[46:47], 0, v[162:163]
	s_mov_b32 m0, s37
	s_nop 0
	global_load_lds_dwordx4 v[22:23], off
	s_mov_b32 m0, s60
	s_nop 0
	global_load_lds_dwordx4 v[24:25], off
	s_waitcnt vmcnt(8)
	s_waitcnt lgkmcnt(0)
	s_barrier
	s_setprio 1
	s_waitcnt lgkmcnt(0)
	v_mfma_scale_f32_16x16x128_f8f6f4 v[94:97], v[2:9], v[198:205], v[94:97], v234, v238 op_sel_hi:[0,0,0]
	v_mfma_scale_f32_16x16x128_f8f6f4 v[90:93], v[10:17], v[198:205], v[90:93], v234, v238 op_sel_hi:[0,0,0]
	v_mfma_scale_f32_16x16x128_f8f6f4 v[86:89], v[2:9], v[206:213], v[86:89], v234, v238 op_sel_hi:[0,0,0]
	v_mfma_scale_f32_16x16x128_f8f6f4 v[82:85], v[10:17], v[206:213], v[82:85], v234, v238 op_sel_hi:[0,0,0]
	v_mfma_scale_f32_16x16x128_f8f6f4 v[78:81], v[2:9], v[216:223], v[78:81], v234, v238 op_sel_hi:[0,0,0]
	v_mfma_scale_f32_16x16x128_f8f6f4 v[74:77], v[10:17], v[216:223], v[74:77], v234, v238 op_sel_hi:[0,0,0]
	v_mfma_scale_f32_16x16x128_f8f6f4 v[70:73], v[2:9], v[224:231], v[70:73], v234, v238 op_sel_hi:[0,0,0]
	v_mfma_scale_f32_16x16x128_f8f6f4 v[66:69], v[10:17], v[224:231], v[66:69], v234, v238 op_sel_hi:[0,0,0]
	v_mfma_scale_f32_16x16x128_f8f6f4 v[62:65], v[26:33], v[198:205], v[62:65], v234, v238 op_sel_hi:[0,0,0]
	v_mfma_scale_f32_16x16x128_f8f6f4 v[58:61], v[172:179], v[198:205], v[58:61], v234, v238 op_sel_hi:[0,0,0]
	v_mfma_scale_f32_16x16x128_f8f6f4 v[54:57], v[26:33], v[206:213], v[54:57], v234, v238 op_sel_hi:[0,0,0]
	v_mfma_scale_f32_16x16x128_f8f6f4 v[50:53], v[172:179], v[206:213], v[50:53], v234, v238 op_sel_hi:[0,0,0]
	v_mfma_scale_f32_16x16x128_f8f6f4 v[46:49], v[26:33], v[216:223], v[46:49], v234, v238 op_sel_hi:[0,0,0]
	v_mfma_scale_f32_16x16x128_f8f6f4 v[42:45], v[172:179], v[216:223], v[42:45], v234, v238 op_sel_hi:[0,0,0]
	v_mfma_scale_f32_16x16x128_f8f6f4 v[38:41], v[26:33], v[224:231], v[38:41], v234, v238 op_sel_hi:[0,0,0]
	v_mfma_scale_f32_16x16x128_f8f6f4 v[34:37], v[172:179], v[224:231], v[34:37], v234, v238 op_sel_hi:[0,0,0]
	s_setprio 0
	s_barrier
	ds_read_b128 v[10:13], v188
	ds_read_b128 v[14:17], v189
	ds_read_b128 v[26:29], v190
	ds_read_b128 v[30:33], v191
	ds_read_b128 v[2:5], v192
	ds_read_b128 v[6:9], v193
	ds_read_b128 v[172:175], v194
	ds_read_b128 v[176:179], v195
	s_add_u32 s46, s46, 0x20000
	s_addc_u32 s47, s47, 0
	s_mov_b32 m0, s61
	v_lshl_add_u64 v[232:233], s[46:47], 0, v[162:163]
	ds_read_b128 v[198:201], v196 offset:32768
	ds_read_b128 v[202:205], v196 offset:33792
	ds_read_b128 v[206:209], v196 offset:34816
	ds_read_b128 v[210:213], v196 offset:35840
	ds_read_b128 v[216:219], v196 offset:36864
	ds_read_b128 v[220:223], v196 offset:37888
	ds_read_b128 v[224:227], v196 offset:38912
	ds_read_b128 v[228:231], v196 offset:39936
	global_load_lds_dwordx4 v[232:233], off
	v_lshl_add_u64 v[232:233], s[46:47], 0, v[164:165]
	s_mov_b32 m0, s62
	s_nop 0
	global_load_lds_dwordx4 v[232:233], off
	s_waitcnt vmcnt(8)
	s_waitcnt lgkmcnt(0)
	s_barrier
	s_setprio 1
	s_waitcnt lgkmcnt(0)
	v_mfma_scale_f32_16x16x128_f8f6f4 v[158:161], v[10:17], v[198:205], v[158:161], v234, v238 op_sel_hi:[0,0,0]
	v_mfma_scale_f32_16x16x128_f8f6f4 v[154:157], v[26:33], v[198:205], v[154:157], v234, v238 op_sel_hi:[0,0,0]
	v_mfma_scale_f32_16x16x128_f8f6f4 v[150:153], v[10:17], v[206:213], v[150:153], v234, v238 op_sel_hi:[0,0,0]
	v_mfma_scale_f32_16x16x128_f8f6f4 v[146:149], v[26:33], v[206:213], v[146:149], v234, v238 op_sel_hi:[0,0,0]
	v_mfma_scale_f32_16x16x128_f8f6f4 v[142:145], v[10:17], v[216:223], v[142:145], v234, v238 op_sel_hi:[0,0,0]
	v_mfma_scale_f32_16x16x128_f8f6f4 v[138:141], v[26:33], v[216:223], v[138:141], v234, v238 op_sel_hi:[0,0,0]
	v_mfma_scale_f32_16x16x128_f8f6f4 v[134:137], v[10:17], v[224:231], v[134:137], v234, v238 op_sel_hi:[0,0,0]
	v_mfma_scale_f32_16x16x128_f8f6f4 v[130:133], v[26:33], v[224:231], v[130:133], v234, v238 op_sel_hi:[0,0,0]
	v_mfma_scale_f32_16x16x128_f8f6f4 v[126:129], v[2:9], v[198:205], v[126:129], v234, v238 op_sel_hi:[0,0,0]
	v_mfma_scale_f32_16x16x128_f8f6f4 v[122:125], v[172:179], v[198:205], v[122:125], v234, v238 op_sel_hi:[0,0,0]
	v_mfma_scale_f32_16x16x128_f8f6f4 v[118:121], v[2:9], v[206:213], v[118:121], v234, v238 op_sel_hi:[0,0,0]
	v_mfma_scale_f32_16x16x128_f8f6f4 v[114:117], v[172:179], v[206:213], v[114:117], v234, v238 op_sel_hi:[0,0,0]
	v_mfma_scale_f32_16x16x128_f8f6f4 v[110:113], v[2:9], v[216:223], v[110:113], v234, v238 op_sel_hi:[0,0,0]
	v_mfma_scale_f32_16x16x128_f8f6f4 v[106:109], v[172:179], v[216:223], v[106:109], v234, v238 op_sel_hi:[0,0,0]
	v_mfma_scale_f32_16x16x128_f8f6f4 v[102:105], v[2:9], v[224:231], v[102:105], v234, v238 op_sel_hi:[0,0,0]
	v_mfma_scale_f32_16x16x128_f8f6f4 v[98:101], v[172:179], v[224:231], v[98:101], v234, v238 op_sel_hi:[0,0,0]
	s_setprio 0
	s_barrier
	s_mov_b32 m0, s65
	v_lshl_add_u64 v[18:19], v[18:19], 0, s[66:67]
	s_add_u32 s44, s44, 0x20080
	ds_read_b128 v[198:201], v196 offset:49152
	ds_read_b128 v[202:205], v196 offset:50176
	ds_read_b128 v[206:209], v196 offset:51200
	ds_read_b128 v[210:213], v196 offset:52224
	ds_read_b128 v[216:219], v196 offset:53248
	ds_read_b128 v[220:223], v196 offset:54272
	ds_read_b128 v[224:227], v196 offset:55296
	ds_read_b128 v[228:231], v196 offset:56320
	global_load_lds_dwordx4 v[18:19], off
	v_lshl_add_u64 v[18:19], v[20:21], 0, s[66:67]
	s_mov_b32 m0, s68
	s_addc_u32 s45, s45, 0
	global_load_lds_dwordx4 v[18:19], off
	v_lshl_add_u64 v[18:19], s[44:45], 0, v[0:1]
	s_mov_b32 m0, s51
	s_nop 0
	global_load_lds_dwordx4 v[18:19], off
	v_lshl_add_u64 v[18:19], s[44:45], 0, v[166:167]
	s_mov_b32 m0, s4
	s_nop 0
	global_load_lds_dwordx4 v[18:19], off
	v_lshl_add_u64 v[18:19], v[22:23], 0, s[66:67]
	s_mov_b32 m0, s81
	s_nop 0
	global_load_lds_dwordx4 v[18:19], off
	v_lshl_add_u64 v[18:19], v[24:25], 0, s[66:67]
	s_mov_b32 m0, s50
	s_nop 0
	global_load_lds_dwordx4 v[18:19], off
	s_waitcnt vmcnt(8)
	s_waitcnt lgkmcnt(0)
	s_barrier
	s_setprio 1
	s_waitcnt lgkmcnt(0)
	v_mfma_scale_f32_16x16x128_f8f6f4 v[94:97], v[10:17], v[198:205], v[94:97], v234, v238 op_sel_hi:[0,0,0]
	v_mfma_scale_f32_16x16x128_f8f6f4 v[90:93], v[26:33], v[198:205], v[90:93], v234, v238 op_sel_hi:[0,0,0]
	v_mfma_scale_f32_16x16x128_f8f6f4 v[86:89], v[10:17], v[206:213], v[86:89], v234, v238 op_sel_hi:[0,0,0]
	v_mfma_scale_f32_16x16x128_f8f6f4 v[82:85], v[26:33], v[206:213], v[82:85], v234, v238 op_sel_hi:[0,0,0]
	v_mfma_scale_f32_16x16x128_f8f6f4 v[78:81], v[10:17], v[216:223], v[78:81], v234, v238 op_sel_hi:[0,0,0]
	v_mfma_scale_f32_16x16x128_f8f6f4 v[74:77], v[26:33], v[216:223], v[74:77], v234, v238 op_sel_hi:[0,0,0]
	v_mfma_scale_f32_16x16x128_f8f6f4 v[70:73], v[10:17], v[224:231], v[70:73], v234, v238 op_sel_hi:[0,0,0]
	v_mfma_scale_f32_16x16x128_f8f6f4 v[66:69], v[26:33], v[224:231], v[66:69], v234, v238 op_sel_hi:[0,0,0]
	v_mfma_scale_f32_16x16x128_f8f6f4 v[62:65], v[2:9], v[198:205], v[62:65], v234, v238 op_sel_hi:[0,0,0]
	v_mfma_scale_f32_16x16x128_f8f6f4 v[58:61], v[172:179], v[198:205], v[58:61], v234, v238 op_sel_hi:[0,0,0]
	v_mfma_scale_f32_16x16x128_f8f6f4 v[54:57], v[2:9], v[206:213], v[54:57], v234, v238 op_sel_hi:[0,0,0]
	v_mfma_scale_f32_16x16x128_f8f6f4 v[50:53], v[172:179], v[206:213], v[50:53], v234, v238 op_sel_hi:[0,0,0]
	v_mfma_scale_f32_16x16x128_f8f6f4 v[46:49], v[2:9], v[216:223], v[46:49], v234, v238 op_sel_hi:[0,0,0]
	v_mfma_scale_f32_16x16x128_f8f6f4 v[42:45], v[172:179], v[216:223], v[42:45], v234, v238 op_sel_hi:[0,0,0]
	v_mfma_scale_f32_16x16x128_f8f6f4 v[38:41], v[2:9], v[224:231], v[38:41], v234, v238 op_sel_hi:[0,0,0]
	v_mfma_scale_f32_16x16x128_f8f6f4 v[34:37], v[172:179], v[224:231], v[34:37], v234, v238 op_sel_hi:[0,0,0]
	s_setprio 0
	s_barrier
	s_add_i32 s74, s74, 2
	s_add_u32 s42, s42, 0x100
	s_addc_u32 s43, s43, 0
	s_add_u32 s48, s48, 0x100
	s_addc_u32 s49, s49, 0
	s_cmp_gt_u32 s74, 5
	s_cbranch_scc0 .LBB0_2089
	s_and_b64 vcc, exec, s[8:9]
	s_cbranch_vccz .LBB0_2092
	s_barrier
